# trailing half takes the restore barrier after the next unit's scalar head; compiler vmcnt(0) in first trips dropped
# baseline (speedup 1.0000x reference)
; #define LAS __attribute__((address_space(3)))
; #define TID fresh_tid()
; __global__ void __launch_bounds__(NWAVES * 64, 2) fwd(Args args) {
;     extern __shared__ __attribute__((aligned(16))) unsigned char lds_raw[];
;     LAS unsigned char* lds = (LAS unsigned char*)lds_raw;
;     volatile LAS unsigned* MISC = (volatile LAS unsigned*)(lds + MISC_OFF);
;     ...
;     const int wave = __builtin_amdgcn_readfirstlane(TID >> 6);
;     const int G = gridDim.x; const int bx = blockIdx.x; const int vcu = (G % 8 == 0) ? (bx % 8) * (G / 8) + bx / 8 : bx;
;     const int gw = vcu * NWAVES + wave, NGW = G * NWAVES;
_Z3fwd4Args:
	v_mov_b32_e32 v212, v0
	s_mov_b32 s98, 0
	s_load_dwordx2 s[18:19], s[0:1], 0xa0
	s_load_dword s12, s[0:1], 0xa8
	s_load_dwordx8 s[4:11], s[0:1], 0x80
	s_mov_b32 s20, s2
	s_waitcnt lgkmcnt(0)
	v_writelane_b32 v252, s4, 0
	s_nop 1
	v_writelane_b32 v252, s5, 1
	v_writelane_b32 v252, s6, 2
	v_writelane_b32 v252, s7, 3
	v_writelane_b32 v252, s8, 4
	v_writelane_b32 v252, s9, 5
	v_writelane_b32 v252, s10, 6
	v_writelane_b32 v252, s11, 7
	s_add_u32 s4, s0, 0xa8
	s_addc_u32 s5, s1, 0
	v_writelane_b32 v252, s4, 8
	s_and_b32 s3, s12, 7
	v_readfirstlane_b32 s6, v0
	v_writelane_b32 v252, s5, 9
	s_mov_b32 s4, s12
	v_writelane_b32 v252, s4, 10
	s_cmp_lg_u32 s3, 0
	s_nop 0
	v_writelane_b32 v252, s5, 11
	v_writelane_b32 v252, s2, 12
	s_cbranch_scc1 .LBB0_2
	s_load_dword s2, s[0:1], 0xa8
	s_ashr_i32 s3, s20, 31
	s_lshr_b32 s3, s3, 29
	s_add_i32 s3, s20, s3
	s_and_b32 s4, s3, -8
	s_waitcnt lgkmcnt(0)
	s_ashr_i32 s2, s2, 3
	s_sub_i32 s4, s20, s4
	s_mul_i32 s2, s2, s4
	s_ashr_i32 s3, s3, 3
	s_add_i32 s2, s2, s3
	v_writelane_b32 v252, s2, 12

;     __device__ bool next(int i, Unit& u) const { const int rounds = nwg / G; if (i >= rounds) return false; return StaticOrder::next(rounds - 1 - i, u); }
;     __device__ bool next(int i, Unit& u) const { const int rounds = nwg / G; if (i >= 2 * rounds) return false; const bool ok = StaticOrder::next(i >= rounds ? i - rounds : i, u); u.z = (i >= rounds) ? 1 : 0; return ok; }
; #define PG8_BAR __builtin_amdgcn_s_barrier()
; #define PG8_TRIP_HEAD(T) const int t = (T); const bool last = (t == nt - 2); \
;             const char* a1 = cA + (size_t)(t + 1) * kstep; \
;             const char* a2 = last ? nA : cA + (size_t)(t + 2) * kstep; const char* b2 = last ? nB : cB + (size_t)(t + 2) * kstep; \
;             const char* a3 = a2 + kstep; const char* b3 = b2 + kstep; \
;             if (last && has_next) S.a_ready(nxt);
; template <class Epi, class Sched, bool ALIGN_EPI = false, bool SP2 = false>
; __device__ __forceinline__ void gemm_phase(PG8_LAS unsigned char* lds, const Gemm g, const Sched& S, const Epi& E) {
;     ...
;         const bool has_next = S.next(ui + 1, nxt);
;         const char* nA = has_next ? (const char*)S.opA(g, nxt) + (size_t)nxt.pm * tstepA : cA; const char* nB = has_next ? (const char*)S.opB(g, nxt) + (size_t)nxt.pn * tstepB : cB;
;     ...
;         if constexpr (SP2) {
;             { PG8_TRIP_HEAD(0) PG8_TRIP_SP2(asm volatile("s_waitcnt vmcnt(%0)" :: "n"(8 + Epi::NST) : "memory"), PG8_MMAZ) }
;     ...
;         if constexpr (ALIGN_EPI) { if (wr == 1) PG8_BAR; }
.LBB0_129:
	s_ashr_i32 s23, s22, 31
	s_lshl_b64 s[4:5], s[22:23], 20
	s_add_u32 s26, s34, s4
	s_addc_u32 s27, s35, s5
	s_cmp_eq_u32 s98, 1
	s_cbranch_scc0 .Llr_gu
	s_barrier
	s_mov_b32 s98, 0
.Llr_gu:
	s_add_i32 s45, 0, 0x10000
	s_add_i32 s47, 0, 0x14000
	v_add_u32_e32 v140, s45, v160
	v_add_u32_e32 v141, s47, v160
	ds_read_b128 v[4:7], v140
	ds_read_b128 v[8:11], v140 offset:1024
	ds_read_b128 v[12:15], v140 offset:2048
	ds_read_b128 v[16:19], v140 offset:3072
	ds_read_b128 v[20:23], v141
	ds_read_b128 v[24:27], v141 offset:1024
	ds_read_b128 v[28:31], v141 offset:2048
	ds_read_b128 v[32:35], v141 offset:3072
	s_and_b64 s[4:5], s[10:11], exec
	s_cselect_b32 s4, s27, s29
	s_cselect_b32 s5, s26, s28
	v_lshl_add_u64 v[184:185], s[30:31], 0, v[134:135]
	s_mov_b64 s[10:11], 0x84080
	s_add_i32 s23, s37, 0xc000
	v_lshl_add_u64 v[68:69], v[184:185], 0, s[10:11]
	s_mov_b32 m0, s23
	s_mov_b64 s[10:11], 0xc6080
	s_add_i32 s33, s37, 0xe000
	ds_read_b128 v[36:39], v163
	ds_read_b128 v[40:43], v163 offset:1024
	ds_read_b128 v[44:47], v163 offset:2048
	ds_read_b128 v[48:51], v163 offset:3072
	ds_read_b128 v[52:55], v163 offset:4096
	ds_read_b128 v[56:59], v163 offset:5120
	ds_read_b128 v[60:63], v163 offset:6144
	ds_read_b128 v[64:67], v163 offset:7168
	global_load_lds_dwordx4 v[68:69], off
	v_lshl_add_u64 v[68:69], v[184:185], 0, s[10:11]
	s_mov_b32 m0, s33
	s_nop 0
	global_load_lds_dwordx4 v[68:69], off
	s_waitcnt vmcnt(16)
	s_waitcnt lgkmcnt(0)
	s_barrier
	s_setprio 1
	s_waitcnt lgkmcnt(0)
	v_mfma_f32_16x16x32_bf16 v[88:91], v[12:15], v[52:55], 0
	v_mfma_f32_16x16x32_bf16 v[92:95], v[16:19], v[56:59], v[88:91]
	v_mfma_f32_16x16x32_bf16 v[88:91], v[4:7], v[60:63], 0
	v_mfma_f32_16x16x32_bf16 v[68:71], v[4:7], v[36:39], 0
	v_mfma_f32_16x16x32_bf16 v[72:75], v[12:15], v[36:39], 0
	v_mfma_f32_16x16x32_bf16 v[76:79], v[4:7], v[44:47], 0
	v_mfma_f32_16x16x32_bf16 v[80:83], v[12:15], v[44:47], 0
	v_mfma_f32_16x16x32_bf16 v[84:87], v[4:7], v[52:55], 0
	v_mfma_f32_16x16x32_bf16 v[96:99], v[8:11], v[64:67], v[88:91]
	v_mfma_f32_16x16x32_bf16 v[88:91], v[12:15], v[60:63], 0
	v_mfma_f32_16x16x32_bf16 v[68:71], v[8:11], v[40:43], v[68:71]
	v_mfma_f32_16x16x32_bf16 v[72:75], v[16:19], v[40:43], v[72:75]
	v_mfma_f32_16x16x32_bf16 v[76:79], v[8:11], v[48:51], v[76:79]
	v_mfma_f32_16x16x32_bf16 v[80:83], v[16:19], v[48:51], v[80:83]
	v_mfma_f32_16x16x32_bf16 v[84:87], v[8:11], v[56:59], v[84:87]
	v_mfma_f32_16x16x32_bf16 v[108:111], v[16:19], v[64:67], v[88:91]
	s_setprio 0
	s_setprio 1
	v_mfma_f32_16x16x32_bf16 v[88:91], v[20:23], v[36:39], 0
	v_mfma_f32_16x16x32_bf16 v[36:39], v[28:31], v[36:39], 0
	v_mfma_f32_16x16x32_bf16 v[112:115], v[24:27], v[40:43], v[88:91]
	v_mfma_f32_16x16x32_bf16 v[36:39], v[32:35], v[40:43], v[36:39]
	v_mfma_f32_16x16x32_bf16 v[40:43], v[20:23], v[44:47], 0
	v_mfma_f32_16x16x32_bf16 v[44:47], v[28:31], v[44:47], 0
	v_mfma_f32_16x16x32_bf16 v[40:43], v[24:27], v[48:51], v[40:43]
	v_mfma_f32_16x16x32_bf16 v[44:47], v[32:35], v[48:51], v[44:47]
	v_mfma_f32_16x16x32_bf16 v[48:51], v[20:23], v[52:55], 0
	v_mfma_f32_16x16x32_bf16 v[52:55], v[28:31], v[52:55], 0
	v_mfma_f32_16x16x32_bf16 v[48:51], v[24:27], v[56:59], v[48:51]
	v_mfma_f32_16x16x32_bf16 v[52:55], v[32:35], v[56:59], v[52:55]
	v_mfma_f32_16x16x32_bf16 v[56:59], v[20:23], v[60:63], 0
	v_mfma_f32_16x16x32_bf16 v[60:63], v[28:31], v[60:63], 0
	v_mfma_f32_16x16x32_bf16 v[56:59], v[24:27], v[64:67], v[56:59]
	v_mfma_f32_16x16x32_bf16 v[60:63], v[32:35], v[64:67], v[60:63]
	s_setprio 0
	s_barrier
	v_lshl_add_u64 v[186:187], s[28:29], 0, v[132:133]
	s_mov_b64 s[10:11], 0x100
	s_add_i32 s45, s45, s36
	v_lshl_add_u64 v[142:143], v[186:187], 0, s[10:11]
	s_mov_b32 m0, s45
	s_mov_b64 s[48:49], 0x40100
	s_add_i32 s46, s45, 0x2000
	ds_read_b128 v[64:67], v163 offset:16384
	ds_read_b128 v[88:91], v163 offset:17408
	ds_read_b128 v[100:103], v163 offset:18432
	ds_read_b128 v[104:107], v163 offset:19456
	ds_read_b128 v[116:119], v163 offset:20480
	ds_read_b128 v[120:123], v163 offset:21504
	ds_read_b128 v[124:127], v163 offset:22528
	ds_read_b128 v[128:131], v163 offset:23552
	global_load_lds_dwordx4 v[142:143], off
	v_lshl_add_u64 v[142:143], v[186:187], 0, s[48:49]
	s_mov_b32 m0, s46
	s_mov_b64 s[48:49], 0x80100
	s_add_i32 s47, s47, s36
	global_load_lds_dwordx4 v[142:143], off
	v_lshl_add_u64 v[142:143], v[186:187], 0, s[48:49]
	s_mov_b32 m0, s47
	s_mov_b64 s[48:49], 0xc0100
	global_load_lds_dwordx4 v[142:143], off
	v_lshl_add_u64 v[142:143], v[186:187], 0, s[48:49]
	s_add_i32 s48, s47, 0x2000
	s_mov_b32 m0, s48
	s_nop 0
	global_load_lds_dwordx4 v[142:143], off
	v_lshl_add_u64 v[142:143], v[184:185], 0, s[10:11]
	s_mov_b32 m0, s37
	s_mov_b64 s[10:11], 0x42100
	global_load_lds_dwordx4 v[142:143], off
	v_lshl_add_u64 v[142:143], v[184:185], 0, s[10:11]
	s_mov_b32 m0, s38
	s_nop 0
	global_load_lds_dwordx4 v[142:143], off
	s_waitcnt vmcnt(16)
	s_waitcnt lgkmcnt(0)
	s_barrier
	s_setprio 1
	s_waitcnt lgkmcnt(0)
	v_mfma_f32_16x16x32_bf16 v[142:145], v[4:7], v[64:67], 0
	v_mfma_f32_16x16x32_bf16 v[152:155], v[4:7], v[100:103], 0
	v_mfma_f32_16x16x32_bf16 v[164:167], v[4:7], v[116:119], 0
	v_mfma_f32_16x16x32_bf16 v[4:7], v[4:7], v[124:127], 0
	v_mfma_f32_16x16x32_bf16 v[144:147], v[8:11], v[88:91], v[142:145]
	v_mfma_f32_16x16x32_bf16 v[152:155], v[8:11], v[104:107], v[152:155]
	v_mfma_f32_16x16x32_bf16 v[164:167], v[8:11], v[120:123], v[164:167]
	v_mfma_f32_16x16x32_bf16 v[4:7], v[8:11], v[128:131], v[4:7]
	v_mfma_f32_16x16x32_bf16 v[8:11], v[12:15], v[124:127], 0
	v_mfma_f32_16x16x32_bf16 v[148:151], v[12:15], v[64:67], 0
	v_mfma_f32_16x16x32_bf16 v[156:159], v[12:15], v[100:103], 0
	v_mfma_f32_16x16x32_bf16 v[168:171], v[12:15], v[116:119], 0
	v_mfma_f32_16x16x32_bf16 v[12:15], v[16:19], v[128:131], v[8:11]
	v_mfma_f32_16x16x32_bf16 v[148:151], v[16:19], v[88:91], v[148:151]
	v_mfma_f32_16x16x32_bf16 v[156:159], v[16:19], v[104:107], v[156:159]
	v_mfma_f32_16x16x32_bf16 v[168:171], v[16:19], v[120:123], v[168:171]
	s_setprio 0
	s_setprio 1
	v_mfma_f32_16x16x32_bf16 v[8:11], v[20:23], v[64:67], 0
	v_mfma_f32_16x16x32_bf16 v[16:19], v[24:27], v[88:91], v[8:11]
	v_mfma_f32_16x16x32_bf16 v[8:11], v[28:31], v[64:67], 0
	v_mfma_f32_16x16x32_bf16 v[172:175], v[32:35], v[88:91], v[8:11]
	v_mfma_f32_16x16x32_bf16 v[8:11], v[20:23], v[100:103], 0
	v_mfma_f32_16x16x32_bf16 v[176:179], v[24:27], v[104:107], v[8:11]
	v_mfma_f32_16x16x32_bf16 v[8:11], v[28:31], v[100:103], 0
	v_mfma_f32_16x16x32_bf16 v[194:197], v[32:35], v[104:107], v[8:11]
	v_mfma_f32_16x16x32_bf16 v[8:11], v[20:23], v[116:119], 0
	v_mfma_f32_16x16x32_bf16 v[198:201], v[24:27], v[120:123], v[8:11]
	v_mfma_f32_16x16x32_bf16 v[8:11], v[28:31], v[116:119], 0
	v_mfma_f32_16x16x32_bf16 v[202:205], v[32:35], v[120:123], v[8:11]
	v_mfma_f32_16x16x32_bf16 v[8:11], v[20:23], v[124:127], 0
	v_mfma_f32_16x16x32_bf16 v[206:209], v[24:27], v[128:131], v[8:11]
	v_mfma_f32_16x16x32_bf16 v[8:11], v[28:31], v[124:127], 0
	v_mfma_f32_16x16x32_bf16 v[220:223], v[32:35], v[128:131], v[8:11]
	s_setprio 0
	s_barrier
	s_add_i32 s49, 0, 0x18000
	s_add_i32 s51, 0, 0x1c000
	v_add_u32_e32 v142, s49, v160
	v_add_u32_e32 v143, s51, v160
	s_nop 0
	ds_read_b128 v[8:11], v142
	ds_read_b128 v[28:31], v142 offset:1024
	ds_read_b128 v[32:35], v142 offset:2048
	ds_read_b128 v[64:67], v142 offset:3072
	ds_read_b128 v[224:227], v143
	ds_read_b128 v[228:231], v143 offset:1024
	ds_read_b128 v[232:235], v143 offset:2048
	ds_read_b128 v[236:239], v143 offset:3072
	s_mov_b64 s[10:11], 0x84100
	s_mov_b32 m0, s39
	v_lshl_add_u64 v[88:89], v[184:185], 0, s[10:11]
	s_mov_b64 s[10:11], 0xc6100
	ds_read_b128 v[20:23], v163 offset:32768
	ds_read_b128 v[24:27], v163 offset:33792
	ds_read_b128 v[240:243], v163 offset:34816
	ds_read_b128 v[244:247], v163 offset:35840
	ds_read_b128 v[248:251], v163 offset:36864
	ds_read_b128 v[216:219], v163 offset:37888
	ds_read_b128 v[190:193], v163 offset:38912
	ds_read_b128 v[180:183], v163 offset:39936
	global_load_lds_dwordx4 v[88:89], off
	v_lshl_add_u64 v[88:89], v[184:185], 0, s[10:11]
	s_mov_b32 m0, s40
	s_nop 0
	global_load_lds_dwordx4 v[88:89], off
	s_waitcnt vmcnt(8)
	s_waitcnt lgkmcnt(0)
	s_barrier
	s_setprio 1
	s_waitcnt lgkmcnt(0)
	v_mfma_f32_16x16x32_bf16 v[68:71], v[8:11], v[20:23], v[68:71]
	v_mfma_f32_16x16x32_bf16 v[120:123], v[28:31], v[24:27], v[68:71]
	v_mfma_f32_16x16x32_bf16 v[68:71], v[32:35], v[20:23], v[72:75]
	v_mfma_f32_16x16x32_bf16 v[116:119], v[64:67], v[24:27], v[68:71]
	v_mfma_f32_16x16x32_bf16 v[68:71], v[8:11], v[240:243], v[76:79]
	v_mfma_f32_16x16x32_bf16 v[104:107], v[28:31], v[244:247], v[68:71]
	v_mfma_f32_16x16x32_bf16 v[68:71], v[32:35], v[240:243], v[80:83]
	v_mfma_f32_16x16x32_bf16 v[100:103], v[64:67], v[244:247], v[68:71]
	v_mfma_f32_16x16x32_bf16 v[68:71], v[8:11], v[248:251], v[84:87]
	v_mfma_f32_16x16x32_bf16 v[88:91], v[28:31], v[216:219], v[68:71]
	v_mfma_f32_16x16x32_bf16 v[68:71], v[32:35], v[248:251], v[92:95]
	v_mfma_f32_16x16x32_bf16 v[84:87], v[64:67], v[216:219], v[68:71]
	v_mfma_f32_16x16x32_bf16 v[68:71], v[8:11], v[190:193], v[96:99]
	v_mfma_f32_16x16x32_bf16 v[72:75], v[28:31], v[180:183], v[68:71]
	v_mfma_f32_16x16x32_bf16 v[68:71], v[32:35], v[190:193], v[108:111]
	v_mfma_f32_16x16x32_bf16 v[68:71], v[64:67], v[180:183], v[68:71]
	s_setprio 0
	s_setprio 1
	v_mfma_f32_16x16x32_bf16 v[76:79], v[224:227], v[20:23], v[112:115]
	v_mfma_f32_16x16x32_bf16 v[20:23], v[232:235], v[20:23], v[36:39]
	v_mfma_f32_16x16x32_bf16 v[124:127], v[236:239], v[24:27], v[20:23]
	v_mfma_f32_16x16x32_bf16 v[20:23], v[224:227], v[240:243], v[40:43]
	v_mfma_f32_16x16x32_bf16 v[112:115], v[228:231], v[244:247], v[20:23]
	v_mfma_f32_16x16x32_bf16 v[20:23], v[232:235], v[240:243], v[44:47]
	v_mfma_f32_16x16x32_bf16 v[108:111], v[236:239], v[244:247], v[20:23]
	v_mfma_f32_16x16x32_bf16 v[20:23], v[224:227], v[248:251], v[48:51]
	v_mfma_f32_16x16x32_bf16 v[96:99], v[228:231], v[216:219], v[20:23]
	v_mfma_f32_16x16x32_bf16 v[20:23], v[232:235], v[248:251], v[52:55]
	v_mfma_f32_16x16x32_bf16 v[92:95], v[236:239], v[216:219], v[20:23]
	v_mfma_f32_16x16x32_bf16 v[20:23], v[224:227], v[190:193], v[56:59]
	v_mfma_f32_16x16x32_bf16 v[80:83], v[228:231], v[180:183], v[20:23]
	v_mfma_f32_16x16x32_bf16 v[20:23], v[232:235], v[190:193], v[60:63]
	v_mfma_f32_16x16x32_bf16 v[128:131], v[228:231], v[24:27], v[76:79]
	v_mfma_f32_16x16x32_bf16 v[76:79], v[236:239], v[180:183], v[20:23]
	s_setprio 0
	s_barrier
; #define PG8_MMA(ai, bj, At, Bt) do { __builtin_amdgcn_s_setprio(1); _Pragma("unroll") for (int m = 0; m < 4; ++m) _Pragma("unroll") for (int n = 0; n < 2; ++n) _Pragma("unroll") for (int k = 0; k < 2; ++k) \
;         acc[ai][bj][m][n] = __builtin_amdgcn_mfma_f32_16x16x32_bf16(Bt[n][k], At[m][k], acc[ai][bj][m][n], 0, 0, 0); __builtin_amdgcn_s_setprio(0); } while (0)
; #define PG8_WAIT_V(n) asm volatile("s_waitcnt vmcnt(" #n ")" ::: "memory")
; #define PG8_TRIP_HEAD(T) const int t = (T); const bool last = (t == nt - 2); \
;             const char* a1 = cA + (size_t)(t + 1) * kstep; \
;             const char* a2 = last ? nA : cA + (size_t)(t + 2) * kstep; const char* b2 = last ? nB : cB + (size_t)(t + 2) * kstep; \
;             const char* a3 = a2 + kstep; const char* b3 = b2 + kstep; \
;             if (last && has_next) S.a_ready(nxt);
; template <class Epi, class Sched, bool ALIGN_EPI = false, bool SP2 = false>
; __device__ __forceinline__ void gemm_phase(PG8_LAS unsigned char* lds, const Gemm g, const Sched& S, const Epi& E) {
;     ...
;         if constexpr (SP2) {
;             { PG8_TRIP_HEAD(0) PG8_TRIP_SP2(asm volatile("s_waitcnt vmcnt(%0)" :: "n"(8 + Epi::NST) : "memory"), PG8_MMAZ) }
;             for (int tt = 2; tt < nt; tt += 2) { PG8_TRIP_HEAD(tt) PG8_TRIP_SP2(PG8_WAIT_V(8), PG8_MMA) }
	s_mov_b64 s[10:11], 0x180
	s_add_i32 s49, s49, s36
	s_nop 1
	v_lshl_add_u64 v[20:21], v[186:187], 0, s[10:11]
	s_mov_b32 m0, s49
	s_mov_b64 s[52:53], 0x40180
	s_add_i32 s50, s49, 0x2000
	ds_read_b128 v[44:47], v163 offset:49152
	ds_read_b128 v[48:51], v163 offset:50176
	ds_read_b128 v[180:183], v163 offset:51200
	ds_read_b128 v[190:193], v163 offset:52224
	ds_read_b128 v[216:219], v163 offset:53248
	ds_read_b128 v[240:243], v163 offset:54272
	ds_read_b128 v[244:247], v163 offset:55296
	ds_read_b128 v[248:251], v163 offset:56320
	global_load_lds_dwordx4 v[20:21], off
	v_lshl_add_u64 v[20:21], v[186:187], 0, s[52:53]
	s_mov_b32 m0, s50
	s_mov_b64 s[52:53], 0x80180
	s_add_i32 s51, s51, s36
	global_load_lds_dwordx4 v[20:21], off
	v_lshl_add_u64 v[20:21], v[186:187], 0, s[52:53]
	s_mov_b32 m0, s51
	s_mov_b64 s[52:53], 0xc0180
	global_load_lds_dwordx4 v[20:21], off
	v_lshl_add_u64 v[20:21], v[186:187], 0, s[52:53]
	s_add_i32 s52, s51, 0x2000
	s_mov_b32 m0, s52
	s_nop 0
	global_load_lds_dwordx4 v[20:21], off
	v_lshl_add_u64 v[20:21], v[184:185], 0, s[10:11]
	s_mov_b32 m0, s0
	s_mov_b64 s[10:11], 0x42180
	global_load_lds_dwordx4 v[20:21], off
	v_lshl_add_u64 v[20:21], v[184:185], 0, s[10:11]
	s_mov_b32 m0, s41
	s_nop 0
	global_load_lds_dwordx4 v[20:21], off
	s_waitcnt vmcnt(8)
	s_waitcnt lgkmcnt(0)
	s_barrier
	s_setprio 1
	s_waitcnt lgkmcnt(0)
	v_mfma_f32_16x16x32_bf16 v[20:23], v[8:11], v[44:47], v[144:147]
	v_mfma_f32_16x16x32_bf16 v[56:59], v[28:31], v[48:51], v[20:23]
	v_mfma_f32_16x16x32_bf16 v[20:23], v[32:35], v[44:47], v[148:151]
	v_mfma_f32_16x16x32_bf16 v[52:55], v[64:67], v[48:51], v[20:23]
	v_mfma_f32_16x16x32_bf16 v[20:23], v[8:11], v[180:183], v[152:155]
	v_mfma_f32_16x16x32_bf16 v[40:43], v[28:31], v[190:193], v[20:23]
	v_mfma_f32_16x16x32_bf16 v[20:23], v[32:35], v[180:183], v[156:159]
	v_mfma_f32_16x16x32_bf16 v[36:39], v[64:67], v[190:193], v[20:23]
	v_mfma_f32_16x16x32_bf16 v[20:23], v[8:11], v[216:219], v[164:167]
	v_mfma_f32_16x16x32_bf16 v[4:7], v[8:11], v[244:247], v[4:7]
	v_mfma_f32_16x16x32_bf16 v[24:27], v[28:31], v[240:243], v[20:23]
	v_mfma_f32_16x16x32_bf16 v[20:23], v[32:35], v[216:219], v[168:171]
	v_mfma_f32_16x16x32_bf16 v[8:11], v[28:31], v[248:251], v[4:7]
	v_mfma_f32_16x16x32_bf16 v[4:7], v[32:35], v[244:247], v[12:15]
	v_mfma_f32_16x16x32_bf16 v[20:23], v[64:67], v[240:243], v[20:23]
	v_mfma_f32_16x16x32_bf16 v[4:7], v[64:67], v[248:251], v[4:7]
	s_setprio 0
	s_setprio 1
	v_mfma_f32_16x16x32_bf16 v[12:15], v[224:227], v[44:47], v[16:19]
	v_mfma_f32_16x16x32_bf16 v[64:67], v[228:231], v[48:51], v[12:15]
	v_mfma_f32_16x16x32_bf16 v[12:15], v[232:235], v[44:47], v[172:175]
	v_mfma_f32_16x16x32_bf16 v[60:63], v[236:239], v[48:51], v[12:15]
	v_mfma_f32_16x16x32_bf16 v[12:15], v[224:227], v[180:183], v[176:179]
	v_mfma_f32_16x16x32_bf16 v[48:51], v[228:231], v[190:193], v[12:15]
	v_mfma_f32_16x16x32_bf16 v[12:15], v[232:235], v[180:183], v[194:197]
	v_mfma_f32_16x16x32_bf16 v[44:47], v[236:239], v[190:193], v[12:15]
	v_mfma_f32_16x16x32_bf16 v[12:15], v[224:227], v[216:219], v[198:201]
	v_mfma_f32_16x16x32_bf16 v[32:35], v[228:231], v[240:243], v[12:15]
	v_mfma_f32_16x16x32_bf16 v[12:15], v[232:235], v[216:219], v[202:205]
	v_mfma_f32_16x16x32_bf16 v[28:31], v[236:239], v[240:243], v[12:15]
	v_mfma_f32_16x16x32_bf16 v[12:15], v[224:227], v[244:247], v[206:209]
	v_mfma_f32_16x16x32_bf16 v[16:19], v[228:231], v[248:251], v[12:15]
	v_mfma_f32_16x16x32_bf16 v[12:15], v[232:235], v[244:247], v[220:223]
	v_mfma_f32_16x16x32_bf16 v[12:15], v[236:239], v[248:251], v[12:15]
	s_setprio 0
	s_barrier
	s_add_u32 s10, s30, 0x84180
	s_addc_u32 s11, s31, 0
	s_add_u32 s28, s28, 0x200
	s_addc_u32 s29, s29, 0
	s_mov_b32 s30, 0
	s_mov_b64 s[60:61], 0x80000
	s_mov_b64 s[62:63], 0x80080
	s_mov_b64 s[64:65], 0xc0000
	s_mov_b64 s[66:67], 0xc0080
	s_mov_b64 s[68:69], 0xc6000

; __device__ __forceinline__ unsigned cvt_pk_bf16(float lo, float hi) { f32x2_c v = {lo, hi}; bf16x2_c b = __builtin_convertvector(v, bf16x2_c); return __builtin_bit_cast(unsigned, b); }
; __device__ __forceinline__ float silu_f(float g) { return g * __builtin_amdgcn_rcpf(1.0f + __builtin_amdgcn_exp2f(-1.44269504f * g)); }
;     __device__ __forceinline__ void operator()(const f32x4 (&acc)[2][2][4][2], const Unit& u, int wr, int wc, int fr, int fq) const {
;     ...
;         for (int ai = 0; ai < 2; ++ai)
; #pragma unroll
;             for (int m = 0; m < 4; ++m) { bf16_t* rowp = O + (size_t)(row0 + ai * HALF + m * 16) * ldc + col0;
;                 const float rs = my[(ai * 4 + m) * 16];
;                 const f32x4 a0 = acc[ai][0][m][0] * rs, a1 = acc[ai][0][m][1] * rs, g0 = acc[ai][1][m][0] * rs, g1 = acc[ai][1][m][1] * rs;
;                 u32x4 w; w.x = cvt_pk_bf16(a0[0] * silu_f(g0[0]), a0[1] * silu_f(g0[1])); w.y = cvt_pk_bf16(a0[2] * silu_f(g0[2]), a0[3] * silu_f(g0[3]));
;                 w.z = cvt_pk_bf16(a1[0] * silu_f(g1[0]), a1[1] * silu_f(g1[1])); w.w = cvt_pk_bf16(a1[2] * silu_f(g1[2]), a1[3] * silu_f(g1[3]));
;                 *(u32x4*)rowp = w; }
.LBB0_153:
	s_waitcnt lgkmcnt(0)
	v_mov_b64_e32 v[142:143], s[94:95]
	s_movk_i32 s4, 0x2c00
	v_lshl_or_b32 v158, s2, 7, v162
	v_mad_u64_u32 v[164:165], s[2:3], v144, s4, v[142:143]
	v_mov_b32_e32 v144, v165
	v_ashrrev_i32_e32 v159, 31, v158
	v_mad_u64_u32 v[144:145], s[2:3], v145, s4, v[144:145]
	v_mov_b32_e32 v165, v144
	v_lshlrev_b64 v[144:145], 1, v[158:159]
	v_lshl_add_u64 v[158:159], v[164:165], 0, v[144:145]
	ds_read2_b32 v[164:165], v161 offset1:16
	s_and_b64 vcc, exec, s[8:9]
	s_waitcnt lgkmcnt(0)
	v_pk_mul_f32 v[166:167], v[118:119], v[164:165] op_sel_hi:[1,0]
	v_pk_mul_f32 v[118:119], v[116:117], v[164:165] op_sel_hi:[1,0]
	v_pk_mul_f32 v[116:117], v[128:129], v[164:165] op_sel_hi:[1,0]
	v_pk_mul_f32 v[120:121], v[120:121], v[164:165] op_sel_hi:[1,0]
	v_mul_f32_e32 v128, 0xbfb8aa3b, v116
	v_mul_f32_e32 v129, 0xbfb8aa3b, v117
	v_exp_f32_e32 v128, v128
	v_exp_f32_e32 v129, v129
	v_pk_mul_f32 v[130:131], v[130:131], v[164:165] op_sel_hi:[1,0]
	v_pk_mul_f32 v[122:123], v[122:123], v[164:165] op_sel_hi:[1,0]
	v_add_f32_e32 v128, 1.0, v128
	v_add_f32_e32 v129, 1.0, v129
	v_rcp_f32_e32 v128, v128
	v_rcp_f32_e32 v129, v129
	v_pk_mul_f32 v[124:125], v[124:125], v[164:165] op_sel_hi:[1,0]
	v_pk_mul_f32 v[126:127], v[126:127], v[164:165] op_sel_hi:[1,0]
	v_pk_mul_f32 v[116:117], v[116:117], v[128:129]
	s_nop 0
	v_pk_mul_f32 v[116:117], v[120:121], v[116:117]
	s_nop 0
	v_cvt_pk_bf16_f32 v116, v116, v117
	v_mul_f32_e32 v117, 0xbfb8aa3b, v130
	v_exp_f32_e32 v117, v117
	s_nop 0
	v_add_f32_e32 v117, 1.0, v117
	v_rcp_f32_e32 v120, v117
	v_mul_f32_e32 v117, 0xbfb8aa3b, v131
	v_exp_f32_e32 v117, v117
	s_nop 0
	v_add_f32_e32 v117, 1.0, v117
	v_rcp_f32_e32 v121, v117
	s_nop 0
	v_pk_mul_f32 v[120:121], v[130:131], v[120:121]
	s_nop 0
	v_pk_mul_f32 v[120:121], v[122:123], v[120:121]
	s_nop 0
	v_cvt_pk_bf16_f32 v117, v120, v121
	v_mul_f32_e32 v120, 0xbfb8aa3b, v124
	v_mul_f32_e32 v121, 0xbfb8aa3b, v125
	v_exp_f32_e32 v120, v120
	v_exp_f32_e32 v121, v121
	v_add_f32_e32 v120, 1.0, v120
	v_add_f32_e32 v121, 1.0, v121
	v_rcp_f32_e32 v120, v120
	v_rcp_f32_e32 v121, v121
	s_nop 0
	v_pk_mul_f32 v[120:121], v[124:125], v[120:121]
	s_nop 0
	v_pk_mul_f32 v[118:119], v[118:119], v[120:121]
	s_nop 0
	v_cvt_pk_bf16_f32 v118, v118, v119
	v_mul_f32_e32 v119, 0xbfb8aa3b, v126
	v_exp_f32_e32 v119, v119
	s_nop 0
	v_add_f32_e32 v119, 1.0, v119
	v_rcp_f32_e32 v120, v119
	v_mul_f32_e32 v119, 0xbfb8aa3b, v127
	v_exp_f32_e32 v119, v119
	s_nop 0
	v_add_f32_e32 v119, 1.0, v119
	v_rcp_f32_e32 v121, v119
	s_nop 0
	v_pk_mul_f32 v[120:121], v[126:127], v[120:121]
	s_nop 0
	v_pk_mul_f32 v[120:121], v[166:167], v[120:121]
	s_nop 0
	v_cvt_pk_bf16_f32 v119, v120, v121
	global_store_dwordx4 v[158:159], v[116:119], off
	s_nop 1
	v_mad_u64_u32 v[116:117], s[2:3], v156, s4, v[142:143]
	v_mov_b32_e32 v118, v117
	v_mad_u64_u32 v[118:119], s[2:3], v157, s4, v[118:119]
	v_mov_b32_e32 v117, v118
	v_mov_b32_e32 v118, v165
	v_pk_mul_f32 v[120:121], v[102:103], v[118:119] op_sel_hi:[1,0]
	v_pk_mul_f32 v[102:103], v[100:101], v[118:119] op_sel_hi:[1,0]
	v_pk_mul_f32 v[100:101], v[112:113], v[118:119] op_sel_hi:[1,0]
	v_pk_mul_f32 v[104:105], v[104:105], v[118:119] op_sel_hi:[1,0]
	v_mul_f32_e32 v112, 0xbfb8aa3b, v100
	v_mul_f32_e32 v113, 0xbfb8aa3b, v101
	v_exp_f32_e32 v112, v112
	v_exp_f32_e32 v113, v113
	v_pk_mul_f32 v[114:115], v[114:115], v[118:119] op_sel_hi:[1,0]
	v_pk_mul_f32 v[106:107], v[106:107], v[118:119] op_sel_hi:[1,0]
	v_add_f32_e32 v112, 1.0, v112
	v_add_f32_e32 v113, 1.0, v113
	v_rcp_f32_e32 v112, v112
	v_rcp_f32_e32 v113, v113
	v_pk_mul_f32 v[108:109], v[108:109], v[118:119] op_sel_hi:[1,0]
	v_pk_mul_f32 v[110:111], v[110:111], v[118:119] op_sel_hi:[1,0]
	v_lshl_add_u64 v[116:117], v[116:117], 0, v[144:145]
	v_pk_mul_f32 v[100:101], v[100:101], v[112:113]
	s_nop 0
	v_pk_mul_f32 v[100:101], v[104:105], v[100:101]
	s_nop 0
	v_cvt_pk_bf16_f32 v100, v100, v101
	v_mul_f32_e32 v101, 0xbfb8aa3b, v114
	v_exp_f32_e32 v101, v101
	s_nop 0
	v_add_f32_e32 v101, 1.0, v101
	v_rcp_f32_e32 v104, v101
	v_mul_f32_e32 v101, 0xbfb8aa3b, v115
	v_exp_f32_e32 v101, v101
	s_nop 0
	v_add_f32_e32 v101, 1.0, v101
	v_rcp_f32_e32 v105, v101
	s_nop 0
	v_pk_mul_f32 v[104:105], v[114:115], v[104:105]
	s_nop 0
	v_pk_mul_f32 v[104:105], v[106:107], v[104:105]
	s_nop 0
	v_cvt_pk_bf16_f32 v101, v104, v105
	v_mul_f32_e32 v104, 0xbfb8aa3b, v108
	v_mul_f32_e32 v105, 0xbfb8aa3b, v109
	v_exp_f32_e32 v104, v104
	v_exp_f32_e32 v105, v105
	v_add_f32_e32 v104, 1.0, v104
	v_add_f32_e32 v105, 1.0, v105
	v_rcp_f32_e32 v104, v104
	v_rcp_f32_e32 v105, v105
	s_nop 0
	v_pk_mul_f32 v[104:105], v[108:109], v[104:105]
	s_nop 0
	v_pk_mul_f32 v[102:103], v[102:103], v[104:105]
	s_nop 0
	v_cvt_pk_bf16_f32 v102, v102, v103
	v_mul_f32_e32 v103, 0xbfb8aa3b, v110
	v_exp_f32_e32 v103, v103
	s_nop 0
	v_add_f32_e32 v103, 1.0, v103
	v_rcp_f32_e32 v104, v103
	v_mul_f32_e32 v103, 0xbfb8aa3b, v111
	v_exp_f32_e32 v103, v103
	s_nop 0
	v_add_f32_e32 v103, 1.0, v103
	v_rcp_f32_e32 v105, v103
	s_nop 0
	v_pk_mul_f32 v[104:105], v[110:111], v[104:105]
	s_nop 0
	v_pk_mul_f32 v[104:105], v[120:121], v[104:105]
	s_nop 0
	v_cvt_pk_bf16_f32 v103, v104, v105
	global_store_dwordx4 v[116:117], v[100:103], off
	s_nop 1
	v_mad_u64_u32 v[100:101], s[2:3], v154, s4, v[142:143]
	v_mov_b32_e32 v102, v101
	v_mad_u64_u32 v[102:103], s[2:3], v155, s4, v[102:103]
	v_mov_b32_e32 v101, v102
	ds_read2_b32 v[102:103], v161 offset0:32 offset1:48
	v_lshl_add_u64 v[100:101], v[100:101], 0, v[144:145]
	s_waitcnt lgkmcnt(0)
; __device__ __forceinline__ unsigned cvt_pk_bf16(float lo, float hi) { f32x2_c v = {lo, hi}; bf16x2_c b = __builtin_convertvector(v, bf16x2_c); return __builtin_bit_cast(unsigned, b); }
; __device__ __forceinline__ float silu_f(float g) { return g * __builtin_amdgcn_rcpf(1.0f + __builtin_amdgcn_exp2f(-1.44269504f * g)); }
;     __device__ __forceinline__ void operator()(const f32x4 (&acc)[2][2][4][2], const Unit& u, int wr, int wc, int fr, int fq) const {
;     ...
;         for (int ai = 0; ai < 2; ++ai)
; #pragma unroll
;             for (int m = 0; m < 4; ++m) { bf16_t* rowp = O + (size_t)(row0 + ai * HALF + m * 16) * ldc + col0;
;                 const float rs = my[(ai * 4 + m) * 16];
;                 const f32x4 a0 = acc[ai][0][m][0] * rs, a1 = acc[ai][0][m][1] * rs, g0 = acc[ai][1][m][0] * rs, g1 = acc[ai][1][m][1] * rs;
;                 u32x4 w; w.x = cvt_pk_bf16(a0[0] * silu_f(g0[0]), a0[1] * silu_f(g0[1])); w.y = cvt_pk_bf16(a0[2] * silu_f(g0[2]), a0[3] * silu_f(g0[3]));
;                 w.z = cvt_pk_bf16(a1[0] * silu_f(g1[0]), a1[1] * silu_f(g1[1])); w.w = cvt_pk_bf16(a1[2] * silu_f(g1[2]), a1[3] * silu_f(g1[3]));
;                 *(u32x4*)rowp = w; }
	v_pk_mul_f32 v[104:105], v[86:87], v[102:103] op_sel_hi:[1,0]
	v_pk_mul_f32 v[86:87], v[84:85], v[102:103] op_sel_hi:[1,0]
	v_pk_mul_f32 v[84:85], v[96:97], v[102:103] op_sel_hi:[1,0]
	v_pk_mul_f32 v[88:89], v[88:89], v[102:103] op_sel_hi:[1,0]
	v_mul_f32_e32 v96, 0xbfb8aa3b, v84
	v_mul_f32_e32 v97, 0xbfb8aa3b, v85
	v_exp_f32_e32 v96, v96
	v_exp_f32_e32 v97, v97
	v_pk_mul_f32 v[98:99], v[98:99], v[102:103] op_sel_hi:[1,0]
	v_pk_mul_f32 v[90:91], v[90:91], v[102:103] op_sel_hi:[1,0]
	v_add_f32_e32 v96, 1.0, v96
	v_add_f32_e32 v97, 1.0, v97
	v_rcp_f32_e32 v96, v96
	v_rcp_f32_e32 v97, v97
	v_pk_mul_f32 v[92:93], v[92:93], v[102:103] op_sel_hi:[1,0]
	v_pk_mul_f32 v[94:95], v[94:95], v[102:103] op_sel_hi:[1,0]
	v_pk_mul_f32 v[84:85], v[84:85], v[96:97]
	s_nop 0
	v_pk_mul_f32 v[84:85], v[88:89], v[84:85]
	s_nop 0
	v_cvt_pk_bf16_f32 v84, v84, v85
	v_mul_f32_e32 v85, 0xbfb8aa3b, v98
	v_exp_f32_e32 v85, v85
	s_nop 0
	v_add_f32_e32 v85, 1.0, v85
	v_rcp_f32_e32 v88, v85
	v_mul_f32_e32 v85, 0xbfb8aa3b, v99
	v_exp_f32_e32 v85, v85
	s_nop 0
	v_add_f32_e32 v85, 1.0, v85
	v_rcp_f32_e32 v89, v85
	s_nop 0
	v_pk_mul_f32 v[88:89], v[98:99], v[88:89]
	s_nop 0
	v_pk_mul_f32 v[88:89], v[90:91], v[88:89]
	s_nop 0
	v_cvt_pk_bf16_f32 v85, v88, v89
	v_mul_f32_e32 v88, 0xbfb8aa3b, v92
	v_mul_f32_e32 v89, 0xbfb8aa3b, v93
	v_exp_f32_e32 v88, v88
	v_exp_f32_e32 v89, v89
	v_add_f32_e32 v88, 1.0, v88
	v_add_f32_e32 v89, 1.0, v89
	v_rcp_f32_e32 v88, v88
	v_rcp_f32_e32 v89, v89
	s_nop 0
	v_pk_mul_f32 v[88:89], v[92:93], v[88:89]
	s_nop 0
	v_pk_mul_f32 v[86:87], v[86:87], v[88:89]
	s_nop 0
	v_cvt_pk_bf16_f32 v86, v86, v87
	v_mul_f32_e32 v87, 0xbfb8aa3b, v94
	v_exp_f32_e32 v87, v87
	s_nop 0
	v_add_f32_e32 v87, 1.0, v87
	v_rcp_f32_e32 v88, v87
	v_mul_f32_e32 v87, 0xbfb8aa3b, v95
	v_exp_f32_e32 v87, v87
	s_nop 0
	v_add_f32_e32 v87, 1.0, v87
	v_rcp_f32_e32 v89, v87
	s_nop 0
	v_pk_mul_f32 v[88:89], v[94:95], v[88:89]
	s_nop 0
	v_pk_mul_f32 v[88:89], v[104:105], v[88:89]
	s_nop 0
	v_cvt_pk_bf16_f32 v87, v88, v89
	global_store_dwordx4 v[100:101], v[84:87], off
	s_nop 1
	v_mad_u64_u32 v[84:85], s[2:3], v152, s4, v[142:143]
	v_mov_b32_e32 v86, v85
	v_mad_u64_u32 v[86:87], s[2:3], v153, s4, v[86:87]
	v_mov_b32_e32 v85, v86
	v_mov_b32_e32 v86, v103
	v_pk_mul_f32 v[88:89], v[70:71], v[86:87] op_sel_hi:[1,0]
	v_pk_mul_f32 v[70:71], v[68:69], v[86:87] op_sel_hi:[1,0]
	v_pk_mul_f32 v[68:69], v[80:81], v[86:87] op_sel_hi:[1,0]
	v_pk_mul_f32 v[72:73], v[72:73], v[86:87] op_sel_hi:[1,0]
	v_mul_f32_e32 v80, 0xbfb8aa3b, v68
	v_mul_f32_e32 v81, 0xbfb8aa3b, v69
	v_exp_f32_e32 v80, v80
	v_exp_f32_e32 v81, v81
	v_pk_mul_f32 v[82:83], v[82:83], v[86:87] op_sel_hi:[1,0]
	v_pk_mul_f32 v[74:75], v[74:75], v[86:87] op_sel_hi:[1,0]
	v_add_f32_e32 v80, 1.0, v80
	v_add_f32_e32 v81, 1.0, v81
	v_rcp_f32_e32 v80, v80
	v_rcp_f32_e32 v81, v81
	v_pk_mul_f32 v[76:77], v[76:77], v[86:87] op_sel_hi:[1,0]
	v_pk_mul_f32 v[78:79], v[78:79], v[86:87] op_sel_hi:[1,0]
	v_lshl_add_u64 v[84:85], v[84:85], 0, v[144:145]
	v_pk_mul_f32 v[68:69], v[68:69], v[80:81]
	s_nop 0
	v_pk_mul_f32 v[68:69], v[72:73], v[68:69]
	s_nop 0
	v_cvt_pk_bf16_f32 v68, v68, v69
	v_mul_f32_e32 v69, 0xbfb8aa3b, v82
	v_exp_f32_e32 v69, v69
	s_nop 0
	v_add_f32_e32 v69, 1.0, v69
	v_rcp_f32_e32 v72, v69
	v_mul_f32_e32 v69, 0xbfb8aa3b, v83
	v_exp_f32_e32 v69, v69
	s_nop 0
	v_add_f32_e32 v69, 1.0, v69
	v_rcp_f32_e32 v73, v69
	s_nop 0
	v_pk_mul_f32 v[72:73], v[82:83], v[72:73]
	s_nop 0
	v_pk_mul_f32 v[72:73], v[74:75], v[72:73]
	s_nop 0
	v_cvt_pk_bf16_f32 v69, v72, v73
	v_mul_f32_e32 v72, 0xbfb8aa3b, v76
	v_mul_f32_e32 v73, 0xbfb8aa3b, v77
	v_exp_f32_e32 v72, v72
	v_exp_f32_e32 v73, v73
	v_add_f32_e32 v72, 1.0, v72
	v_add_f32_e32 v73, 1.0, v73
	v_rcp_f32_e32 v72, v72
	v_rcp_f32_e32 v73, v73
	s_nop 0
	v_pk_mul_f32 v[72:73], v[76:77], v[72:73]
	s_nop 0
	v_pk_mul_f32 v[70:71], v[70:71], v[72:73]
	s_nop 0
	v_cvt_pk_bf16_f32 v70, v70, v71
	v_mul_f32_e32 v71, 0xbfb8aa3b, v78
	v_exp_f32_e32 v71, v71
	s_nop 0
	v_add_f32_e32 v71, 1.0, v71
	v_rcp_f32_e32 v72, v71
	v_mul_f32_e32 v71, 0xbfb8aa3b, v79
	v_exp_f32_e32 v71, v71
	s_nop 0
	v_add_f32_e32 v71, 1.0, v71
	v_rcp_f32_e32 v73, v71
	s_nop 0
	v_pk_mul_f32 v[72:73], v[78:79], v[72:73]
	s_nop 0
	v_pk_mul_f32 v[72:73], v[88:89], v[72:73]
	s_nop 0
	v_cvt_pk_bf16_f32 v71, v72, v73
	global_store_dwordx4 v[84:85], v[68:71], off
	s_nop 1
	v_mad_u64_u32 v[68:69], s[2:3], v150, s4, v[142:143]
	v_mov_b32_e32 v70, v69
	v_mad_u64_u32 v[70:71], s[2:3], v151, s4, v[70:71]
	v_mov_b32_e32 v69, v70
	ds_read2_b32 v[70:71], v161 offset0:64 offset1:80
	v_lshl_add_u64 v[68:69], v[68:69], 0, v[144:145]
	s_waitcnt lgkmcnt(0)
; __device__ __forceinline__ unsigned cvt_pk_bf16(float lo, float hi) { f32x2_c v = {lo, hi}; bf16x2_c b = __builtin_convertvector(v, bf16x2_c); return __builtin_bit_cast(unsigned, b); }
; __device__ __forceinline__ float silu_f(float g) { return g * __builtin_amdgcn_rcpf(1.0f + __builtin_amdgcn_exp2f(-1.44269504f * g)); }
;     __device__ __forceinline__ void operator()(const f32x4 (&acc)[2][2][4][2], const Unit& u, int wr, int wc, int fr, int fq) const {
;     ...
;         for (int ai = 0; ai < 2; ++ai)
; #pragma unroll
;             for (int m = 0; m < 4; ++m) { bf16_t* rowp = O + (size_t)(row0 + ai * HALF + m * 16) * ldc + col0;
;                 const float rs = my[(ai * 4 + m) * 16];
;                 const f32x4 a0 = acc[ai][0][m][0] * rs, a1 = acc[ai][0][m][1] * rs, g0 = acc[ai][1][m][0] * rs, g1 = acc[ai][1][m][1] * rs;
;                 u32x4 w; w.x = cvt_pk_bf16(a0[0] * silu_f(g0[0]), a0[1] * silu_f(g0[1])); w.y = cvt_pk_bf16(a0[2] * silu_f(g0[2]), a0[3] * silu_f(g0[3]));
;                 w.z = cvt_pk_bf16(a1[0] * silu_f(g1[0]), a1[1] * silu_f(g1[1])); w.w = cvt_pk_bf16(a1[2] * silu_f(g1[2]), a1[3] * silu_f(g1[3]));
;                 *(u32x4*)rowp = w; }
	v_pk_mul_f32 v[72:73], v[54:55], v[70:71] op_sel_hi:[1,0]
	v_pk_mul_f32 v[54:55], v[52:53], v[70:71] op_sel_hi:[1,0]
	v_pk_mul_f32 v[52:53], v[64:65], v[70:71] op_sel_hi:[1,0]
	v_pk_mul_f32 v[56:57], v[56:57], v[70:71] op_sel_hi:[1,0]
	v_mul_f32_e32 v64, 0xbfb8aa3b, v52
	v_mul_f32_e32 v65, 0xbfb8aa3b, v53
	v_exp_f32_e32 v64, v64
	v_exp_f32_e32 v65, v65
	v_pk_mul_f32 v[66:67], v[66:67], v[70:71] op_sel_hi:[1,0]
	v_pk_mul_f32 v[58:59], v[58:59], v[70:71] op_sel_hi:[1,0]
	v_add_f32_e32 v64, 1.0, v64
	v_add_f32_e32 v65, 1.0, v65
	v_rcp_f32_e32 v64, v64
	v_rcp_f32_e32 v65, v65
	v_pk_mul_f32 v[60:61], v[60:61], v[70:71] op_sel_hi:[1,0]
	v_pk_mul_f32 v[62:63], v[62:63], v[70:71] op_sel_hi:[1,0]
	v_pk_mul_f32 v[52:53], v[52:53], v[64:65]
	s_nop 0
	v_pk_mul_f32 v[52:53], v[56:57], v[52:53]
	s_nop 0
	v_cvt_pk_bf16_f32 v52, v52, v53
	v_mul_f32_e32 v53, 0xbfb8aa3b, v66
	v_exp_f32_e32 v53, v53
	s_nop 0
	v_add_f32_e32 v53, 1.0, v53
	v_rcp_f32_e32 v56, v53
	v_mul_f32_e32 v53, 0xbfb8aa3b, v67
	v_exp_f32_e32 v53, v53
	s_nop 0
	v_add_f32_e32 v53, 1.0, v53
	v_rcp_f32_e32 v57, v53
	s_nop 0
	v_pk_mul_f32 v[56:57], v[66:67], v[56:57]
	s_nop 0
	v_pk_mul_f32 v[56:57], v[58:59], v[56:57]
	s_nop 0
	v_cvt_pk_bf16_f32 v53, v56, v57
	v_mul_f32_e32 v56, 0xbfb8aa3b, v60
	v_mul_f32_e32 v57, 0xbfb8aa3b, v61
	v_exp_f32_e32 v56, v56
	v_exp_f32_e32 v57, v57
	v_add_f32_e32 v56, 1.0, v56
	v_add_f32_e32 v57, 1.0, v57
	v_rcp_f32_e32 v56, v56
	v_rcp_f32_e32 v57, v57
	s_nop 0
	v_pk_mul_f32 v[56:57], v[60:61], v[56:57]
	s_nop 0
	v_pk_mul_f32 v[54:55], v[54:55], v[56:57]
	s_nop 0
	v_cvt_pk_bf16_f32 v54, v54, v55
	v_mul_f32_e32 v55, 0xbfb8aa3b, v62
	v_exp_f32_e32 v55, v55
	s_nop 0
	v_add_f32_e32 v55, 1.0, v55
	v_rcp_f32_e32 v56, v55
	v_mul_f32_e32 v55, 0xbfb8aa3b, v63
	v_exp_f32_e32 v55, v55
	s_nop 0
	v_add_f32_e32 v55, 1.0, v55
	v_rcp_f32_e32 v57, v55
	s_nop 0
	v_pk_mul_f32 v[56:57], v[62:63], v[56:57]
	s_nop 0
	v_pk_mul_f32 v[56:57], v[72:73], v[56:57]
	s_nop 0
	v_cvt_pk_bf16_f32 v55, v56, v57
	global_store_dwordx4 v[68:69], v[52:55], off
	s_nop 1
	v_mad_u64_u32 v[52:53], s[2:3], v148, s4, v[142:143]
	v_mov_b32_e32 v54, v53
	v_mad_u64_u32 v[54:55], s[2:3], v149, s4, v[54:55]
	v_mov_b32_e32 v53, v54
	v_mov_b32_e32 v54, v71
	v_pk_mul_f32 v[56:57], v[38:39], v[54:55] op_sel_hi:[1,0]
	v_pk_mul_f32 v[38:39], v[36:37], v[54:55] op_sel_hi:[1,0]
	v_pk_mul_f32 v[36:37], v[48:49], v[54:55] op_sel_hi:[1,0]
	v_pk_mul_f32 v[40:41], v[40:41], v[54:55] op_sel_hi:[1,0]
	v_mul_f32_e32 v48, 0xbfb8aa3b, v36
	v_mul_f32_e32 v49, 0xbfb8aa3b, v37
	v_exp_f32_e32 v48, v48
	v_exp_f32_e32 v49, v49
	v_pk_mul_f32 v[50:51], v[50:51], v[54:55] op_sel_hi:[1,0]
	v_pk_mul_f32 v[42:43], v[42:43], v[54:55] op_sel_hi:[1,0]
	v_add_f32_e32 v48, 1.0, v48
	v_add_f32_e32 v49, 1.0, v49
	v_rcp_f32_e32 v48, v48
	v_rcp_f32_e32 v49, v49
	v_pk_mul_f32 v[44:45], v[44:45], v[54:55] op_sel_hi:[1,0]
	v_pk_mul_f32 v[46:47], v[46:47], v[54:55] op_sel_hi:[1,0]
	v_lshl_add_u64 v[52:53], v[52:53], 0, v[144:145]
	v_pk_mul_f32 v[36:37], v[36:37], v[48:49]
	s_nop 0
	v_pk_mul_f32 v[36:37], v[40:41], v[36:37]
	s_nop 0
	v_cvt_pk_bf16_f32 v36, v36, v37
	v_mul_f32_e32 v37, 0xbfb8aa3b, v50
	v_exp_f32_e32 v37, v37
	s_nop 0
	v_add_f32_e32 v37, 1.0, v37
	v_rcp_f32_e32 v40, v37
	v_mul_f32_e32 v37, 0xbfb8aa3b, v51
	v_exp_f32_e32 v37, v37
	s_nop 0
	v_add_f32_e32 v37, 1.0, v37
	v_rcp_f32_e32 v41, v37
	s_nop 0
	v_pk_mul_f32 v[40:41], v[50:51], v[40:41]
	s_nop 0
	v_pk_mul_f32 v[40:41], v[42:43], v[40:41]
	s_nop 0
	v_cvt_pk_bf16_f32 v37, v40, v41
	v_mul_f32_e32 v40, 0xbfb8aa3b, v44
	v_mul_f32_e32 v41, 0xbfb8aa3b, v45
	v_exp_f32_e32 v40, v40
	v_exp_f32_e32 v41, v41
	v_add_f32_e32 v40, 1.0, v40
	v_add_f32_e32 v41, 1.0, v41
	v_rcp_f32_e32 v40, v40
	v_rcp_f32_e32 v41, v41
	s_nop 0
	v_pk_mul_f32 v[40:41], v[44:45], v[40:41]
	s_nop 0
	v_pk_mul_f32 v[38:39], v[38:39], v[40:41]
	s_nop 0
	v_cvt_pk_bf16_f32 v38, v38, v39
	v_mul_f32_e32 v39, 0xbfb8aa3b, v46
	v_exp_f32_e32 v39, v39
	s_nop 0
	v_add_f32_e32 v39, 1.0, v39
	v_rcp_f32_e32 v40, v39
	v_mul_f32_e32 v39, 0xbfb8aa3b, v47
	v_exp_f32_e32 v39, v39
	s_nop 0
	v_add_f32_e32 v39, 1.0, v39
	v_rcp_f32_e32 v41, v39
	s_nop 0
	v_pk_mul_f32 v[40:41], v[46:47], v[40:41]
	s_nop 0
	v_pk_mul_f32 v[40:41], v[56:57], v[40:41]
	s_nop 0
	v_cvt_pk_bf16_f32 v39, v40, v41
	global_store_dwordx4 v[52:53], v[36:39], off
	s_nop 1
	v_mad_u64_u32 v[36:37], s[2:3], v146, s4, v[142:143]
	v_mov_b32_e32 v38, v37
	v_mad_u64_u32 v[38:39], s[2:3], v147, s4, v[38:39]
	v_mov_b32_e32 v37, v38
	ds_read2_b32 v[38:39], v161 offset0:96 offset1:112
	v_lshl_add_u64 v[36:37], v[36:37], 0, v[144:145]
	s_waitcnt lgkmcnt(0)
; __device__ __forceinline__ unsigned cvt_pk_bf16(float lo, float hi) { f32x2_c v = {lo, hi}; bf16x2_c b = __builtin_convertvector(v, bf16x2_c); return __builtin_bit_cast(unsigned, b); }
; __device__ __forceinline__ float silu_f(float g) { return g * __builtin_amdgcn_rcpf(1.0f + __builtin_amdgcn_exp2f(-1.44269504f * g)); }
; #define PG8_BAR __builtin_amdgcn_s_barrier()
;     __device__ __forceinline__ void operator()(const f32x4 (&acc)[2][2][4][2], const Unit& u, int wr, int wc, int fr, int fq) const {
;     ...
;             for (int m = 0; m < 4; ++m) { bf16_t* rowp = O + (size_t)(row0 + ai * HALF + m * 16) * ldc + col0;
;                 const float rs = my[(ai * 4 + m) * 16];
;                 const f32x4 a0 = acc[ai][0][m][0] * rs, a1 = acc[ai][0][m][1] * rs, g0 = acc[ai][1][m][0] * rs, g1 = acc[ai][1][m][1] * rs;
;                 u32x4 w; w.x = cvt_pk_bf16(a0[0] * silu_f(g0[0]), a0[1] * silu_f(g0[1])); w.y = cvt_pk_bf16(a0[2] * silu_f(g0[2]), a0[3] * silu_f(g0[3]));
;                 w.z = cvt_pk_bf16(a1[0] * silu_f(g1[0]), a1[1] * silu_f(g1[1])); w.w = cvt_pk_bf16(a1[2] * silu_f(g1[2]), a1[3] * silu_f(g1[3]));
;                 *(u32x4*)rowp = w; }
; template <class Epi, class Sched, bool ALIGN_EPI = false, bool SP2 = false>
; __device__ __forceinline__ void gemm_phase(PG8_LAS unsigned char* lds, const Gemm g, const Sched& S, const Epi& E) {
;     ...
;         cur = nxt; cA = nA; cB = nB; ++ui;
;         if constexpr (ALIGN_EPI) { if (wr == 1) PG8_BAR; }
	v_pk_mul_f32 v[40:41], v[22:23], v[38:39] op_sel_hi:[1,0]
	v_pk_mul_f32 v[22:23], v[20:21], v[38:39] op_sel_hi:[1,0]
	v_pk_mul_f32 v[20:21], v[32:33], v[38:39] op_sel_hi:[1,0]
	v_pk_mul_f32 v[24:25], v[24:25], v[38:39] op_sel_hi:[1,0]
	v_mul_f32_e32 v32, 0xbfb8aa3b, v20
	v_mul_f32_e32 v33, 0xbfb8aa3b, v21
	v_exp_f32_e32 v32, v32
	v_exp_f32_e32 v33, v33
	v_pk_mul_f32 v[34:35], v[34:35], v[38:39] op_sel_hi:[1,0]
	v_pk_mul_f32 v[26:27], v[26:27], v[38:39] op_sel_hi:[1,0]
	v_add_f32_e32 v32, 1.0, v32
	v_add_f32_e32 v33, 1.0, v33
	v_rcp_f32_e32 v32, v32
	v_rcp_f32_e32 v33, v33
	v_pk_mul_f32 v[28:29], v[28:29], v[38:39] op_sel_hi:[1,0]
	v_pk_mul_f32 v[30:31], v[30:31], v[38:39] op_sel_hi:[1,0]
	v_pk_mul_f32 v[20:21], v[20:21], v[32:33]
	s_nop 0
	v_pk_mul_f32 v[20:21], v[24:25], v[20:21]
	s_nop 0
	v_cvt_pk_bf16_f32 v20, v20, v21
	v_mul_f32_e32 v21, 0xbfb8aa3b, v34
	v_exp_f32_e32 v21, v21
	s_nop 0
	v_add_f32_e32 v21, 1.0, v21
	v_rcp_f32_e32 v24, v21
	v_mul_f32_e32 v21, 0xbfb8aa3b, v35
	v_exp_f32_e32 v21, v21
	s_nop 0
	v_add_f32_e32 v21, 1.0, v21
	v_rcp_f32_e32 v25, v21
	s_nop 0
	v_pk_mul_f32 v[24:25], v[34:35], v[24:25]
	s_nop 0
	v_pk_mul_f32 v[24:25], v[26:27], v[24:25]
	s_nop 0
	v_cvt_pk_bf16_f32 v21, v24, v25
	v_mul_f32_e32 v24, 0xbfb8aa3b, v28
	v_mul_f32_e32 v25, 0xbfb8aa3b, v29
	v_exp_f32_e32 v24, v24
	v_exp_f32_e32 v25, v25
	v_add_f32_e32 v24, 1.0, v24
	v_add_f32_e32 v25, 1.0, v25
	v_rcp_f32_e32 v24, v24
	v_rcp_f32_e32 v25, v25
	s_nop 0
	v_pk_mul_f32 v[24:25], v[28:29], v[24:25]
	s_nop 0
	v_pk_mul_f32 v[22:23], v[22:23], v[24:25]
	s_nop 0
	v_cvt_pk_bf16_f32 v22, v22, v23
	v_mul_f32_e32 v23, 0xbfb8aa3b, v30
	v_exp_f32_e32 v23, v23
	s_nop 0
	v_add_f32_e32 v23, 1.0, v23
	v_rcp_f32_e32 v24, v23
	v_mul_f32_e32 v23, 0xbfb8aa3b, v31
	v_exp_f32_e32 v23, v23
	s_nop 0
	v_add_f32_e32 v23, 1.0, v23
	v_rcp_f32_e32 v25, v23
	s_nop 0
	v_pk_mul_f32 v[24:25], v[30:31], v[24:25]
	s_nop 0
	v_pk_mul_f32 v[24:25], v[40:41], v[24:25]
	s_nop 0
	v_cvt_pk_bf16_f32 v23, v24, v25
	global_store_dwordx4 v[36:37], v[20:23], off
	s_nop 1
	v_mad_u64_u32 v[20:21], s[2:3], v140, s4, v[142:143]
	v_mov_b32_e32 v22, v21
	v_mad_u64_u32 v[22:23], s[2:3], v141, s4, v[22:23]
	v_mov_b32_e32 v21, v22
	v_mov_b32_e32 v22, v39
	v_pk_mul_f32 v[24:25], v[6:7], v[22:23] op_sel_hi:[1,0]
	v_pk_mul_f32 v[6:7], v[4:5], v[22:23] op_sel_hi:[1,0]
	v_pk_mul_f32 v[4:5], v[16:17], v[22:23] op_sel_hi:[1,0]
	v_pk_mul_f32 v[8:9], v[8:9], v[22:23] op_sel_hi:[1,0]
	v_mul_f32_e32 v16, 0xbfb8aa3b, v4
	v_mul_f32_e32 v17, 0xbfb8aa3b, v5
	v_exp_f32_e32 v16, v16
	v_exp_f32_e32 v17, v17
	v_pk_mul_f32 v[18:19], v[18:19], v[22:23] op_sel_hi:[1,0]
	v_pk_mul_f32 v[10:11], v[10:11], v[22:23] op_sel_hi:[1,0]
	v_add_f32_e32 v16, 1.0, v16
	v_add_f32_e32 v17, 1.0, v17
	v_rcp_f32_e32 v16, v16
	v_rcp_f32_e32 v17, v17
	v_pk_mul_f32 v[12:13], v[12:13], v[22:23] op_sel_hi:[1,0]
	v_pk_mul_f32 v[14:15], v[14:15], v[22:23] op_sel_hi:[1,0]
	v_lshl_add_u64 v[20:21], v[20:21], 0, v[144:145]
	v_pk_mul_f32 v[4:5], v[4:5], v[16:17]
	s_mov_b64 s[4:5], -1
	v_pk_mul_f32 v[4:5], v[8:9], v[4:5]
	s_nop 0
	v_cvt_pk_bf16_f32 v4, v4, v5
	v_mul_f32_e32 v5, 0xbfb8aa3b, v18
	v_exp_f32_e32 v5, v5
	s_nop 0
	v_add_f32_e32 v5, 1.0, v5
	v_rcp_f32_e32 v8, v5
	v_mul_f32_e32 v5, 0xbfb8aa3b, v19
	v_exp_f32_e32 v5, v5
	s_nop 0
	v_add_f32_e32 v5, 1.0, v5
	v_rcp_f32_e32 v9, v5
	s_nop 0
	v_pk_mul_f32 v[8:9], v[18:19], v[8:9]
	s_nop 0
	v_pk_mul_f32 v[8:9], v[10:11], v[8:9]
	s_nop 0
	v_cvt_pk_bf16_f32 v5, v8, v9
	v_mul_f32_e32 v8, 0xbfb8aa3b, v12
	v_mul_f32_e32 v9, 0xbfb8aa3b, v13
	v_exp_f32_e32 v8, v8
	v_exp_f32_e32 v9, v9
	v_add_f32_e32 v8, 1.0, v8
	v_add_f32_e32 v9, 1.0, v9
	v_rcp_f32_e32 v8, v8
	v_rcp_f32_e32 v9, v9
	s_nop 0
	v_pk_mul_f32 v[8:9], v[12:13], v[8:9]
	s_nop 0
	v_pk_mul_f32 v[6:7], v[6:7], v[8:9]
	s_nop 0
	v_cvt_pk_bf16_f32 v6, v6, v7
	v_mul_f32_e32 v7, 0xbfb8aa3b, v14
	v_exp_f32_e32 v7, v7
	s_nop 0
	v_add_f32_e32 v7, 1.0, v7
	v_rcp_f32_e32 v8, v7
	v_mul_f32_e32 v7, 0xbfb8aa3b, v15
	v_exp_f32_e32 v7, v7
	s_nop 0
	v_add_f32_e32 v7, 1.0, v7
	v_rcp_f32_e32 v9, v7
	s_nop 0
	v_pk_mul_f32 v[8:9], v[14:15], v[8:9]
	s_nop 0
	v_pk_mul_f32 v[8:9], v[24:25], v[8:9]
	s_nop 0
	v_cvt_pk_bf16_f32 v7, v8, v9
	global_store_dwordx4 v[20:21], v[4:7], off
	s_cbranch_vccnz .LBB0_124
	s_andn2_b64 vcc, exec, s[18:19]
	s_cbranch_vccnz .LBB0_123
	s_mov_b32 s98, 1
	s_branch .LBB0_123

; #define PG8_BAR __builtin_amdgcn_s_barrier()
; template <class Epi, class Sched, bool ALIGN_EPI = false, bool SP2 = false>
; __device__ __forceinline__ void gemm_phase(PG8_LAS unsigned char* lds, const Gemm g, const Sched& S, const Epi& E) {
;     ...
;         if constexpr (ALIGN_EPI) { if (wr == 1) PG8_BAR; }
.LBB0_232:
	s_cmp_eq_u32 s98, 1
	s_cbranch_scc0 .Llr_down
	s_barrier
	s_mov_b32 s98, 0

; #define PG8_BAR __builtin_amdgcn_s_barrier()
;     __device__ __forceinline__ void operator()(const f32x4 (&acc)[2][2][4][2], const Unit& u, int wr, int wc, int fr, int fq) const {
;     ...
;             { const float sv = (fq == 0) ? ssm[0] : (fq == 1) ? ssm[1] : (fq == 2) ? ssm[2] : ssm[3];
;               ssq[(size_t)(row0 + ai * HALF + fq * 16) * 32 + u.pn * 4 + wc] = sv; }
; template <class Epi, class Sched, bool ALIGN_EPI = false, bool SP2 = false>
; __device__ __forceinline__ void gemm_phase(PG8_LAS unsigned char* lds, const Gemm g, const Sched& S, const Epi& E) {
;     ...
;         if (!has_next) break;
;         if constexpr (!SP2) {
; #pragma unroll
;         for (int a = 0; a < 2; ++a)
; #pragma unroll
;             for (int b = 0; b < 2; ++b)
; #pragma unroll
;                 for (int m = 0; m < 4; ++m)
; #pragma unroll
;                     for (int n = 0; n < 2; ++n) acc[a][b][m][n] = (f32x4){0.f, 0.f, 0.f, 0.f};
;         }
;         cur = nxt; cA = nA; cB = nB; ++ui;
;         if constexpr (ALIGN_EPI) { if (wr == 1) PG8_BAR; }
.LBB0_252:
	s_or_b64 exec, exec, s[4:5]
	s_waitcnt lgkmcnt(0)
	v_add_u32_e32 v6, 0x80, v92
	v_ashrrev_i32_e32 v7, 31, v6
	v_lshlrev_b64 v[6:7], 7, v[6:7]
	v_lshl_add_u64 v[6:7], s[16:17], 0, v[6:7]
	v_lshl_add_u64 v[6:7], s[24:25], 2, v[6:7]
	v_lshl_add_u64 v[6:7], v[6:7], 0, s[0:1]
	global_store_dword v[6:7], v4, off
	s_and_b64 vcc, exec, s[8:9]
	s_mov_b64 s[4:5], -1
	s_cbranch_vccnz .LBB0_220
	s_andn2_b64 vcc, exec, s[10:11]
	s_cbranch_vccnz .LBB0_219
	s_mov_b32 s98, 1
	s_branch .LBB0_219

;     __device__ bool next(int i, Unit& u) const { const int rounds = nwg / G; if (i >= rounds) return false; return StaticOrder::next(rounds - 1 - i, u); }
;     __device__ bool next(int i, Unit& u) const { const int rounds = nwg / G; if (i >= 2 * rounds) return false; const bool ok = StaticOrder::next(i >= rounds ? i - rounds : i, u); u.z = (i >= rounds) ? 1 : 0; return ok; }
; template <class Epi, class Sched, bool ALIGN_EPI = false, bool SP2 = false>
; __device__ __forceinline__ void gemm_phase(PG8_LAS unsigned char* lds, const Gemm g, const Sched& S, const Epi& E) {
;     ...
;         const bool has_next = S.next(ui + 1, nxt);
;         const char* nA = has_next ? (const char*)S.opA(g, nxt) + (size_t)nxt.pm * tstepA : cA; const char* nB = has_next ? (const char*)S.opB(g, nxt) + (size_t)nxt.pn * tstepB : cB;
.LBB0_323:
	s_ashr_i32 s23, s22, 31
	s_lshl_b64 s[4:5], s[22:23], 20
	v_readlane_b32 s26, v254, 18
	v_readlane_b32 s27, v254, 19
	s_add_u32 s26, s26, s4
	s_addc_u32 s27, s27, s5
	s_cmp_eq_u32 s98, 1
	s_cbranch_scc0 .Llr_in
	s_barrier
	s_mov_b32 s98, 0
.Llr_in:
	s_add_i32 s28, 0, 0x10000
	s_add_i32 s33, 0, 0x14000
	v_add_u32_e32 v132, s28, v197
	s_waitcnt lgkmcnt(0)
	v_add_u32_e32 v133, s33, v197
	ds_read_b128 v[4:7], v132
	ds_read_b128 v[8:11], v132 offset:1024
	ds_read_b128 v[12:15], v132 offset:2048
	ds_read_b128 v[16:19], v132 offset:3072
	ds_read_b128 v[20:23], v133
	ds_read_b128 v[24:27], v133 offset:1024
	ds_read_b128 v[28:31], v133 offset:2048
	ds_read_b128 v[32:35], v133 offset:3072
	s_and_b64 s[4:5], s[10:11], exec
	s_cselect_b32 s3, s27, s13
	s_cselect_b32 s4, s26, s12
	v_lshl_add_u64 v[194:195], s[14:15], 0, v[166:167]
	s_mov_b64 s[10:11], 0x84080
	s_add_i32 s5, s30, 0xc000
	v_lshl_add_u64 v[68:69], v[194:195], 0, s[10:11]
	s_mov_b32 m0, s5
	s_mov_b64 s[10:11], 0xc6080
	s_add_i32 s23, s30, 0xe000
	ds_read_b128 v[36:39], v200
	ds_read_b128 v[40:43], v200 offset:1024
	ds_read_b128 v[44:47], v200 offset:2048
	ds_read_b128 v[48:51], v200 offset:3072
	ds_read_b128 v[52:55], v200 offset:4096
	ds_read_b128 v[56:59], v200 offset:5120
	ds_read_b128 v[60:63], v200 offset:6144
	ds_read_b128 v[64:67], v200 offset:7168
	global_load_lds_dwordx4 v[68:69], off
	v_lshl_add_u64 v[68:69], v[194:195], 0, s[10:11]
	s_mov_b32 m0, s23
	s_nop 0
	global_load_lds_dwordx4 v[68:69], off
	s_waitcnt vmcnt(16)
	s_waitcnt lgkmcnt(0)
	s_barrier
	s_setprio 1
	s_waitcnt lgkmcnt(0)
	v_mfma_f32_16x16x32_bf16 v[88:91], v[12:15], v[52:55], 0
	v_mfma_f32_16x16x32_bf16 v[92:95], v[16:19], v[56:59], v[88:91]
	v_mfma_f32_16x16x32_bf16 v[88:91], v[4:7], v[60:63], 0
	v_mfma_f32_16x16x32_bf16 v[68:71], v[4:7], v[36:39], 0
	v_mfma_f32_16x16x32_bf16 v[72:75], v[12:15], v[36:39], 0
	v_mfma_f32_16x16x32_bf16 v[76:79], v[4:7], v[44:47], 0
	v_mfma_f32_16x16x32_bf16 v[80:83], v[12:15], v[44:47], 0
	v_mfma_f32_16x16x32_bf16 v[84:87], v[4:7], v[52:55], 0
	v_mfma_f32_16x16x32_bf16 v[96:99], v[8:11], v[64:67], v[88:91]
	v_mfma_f32_16x16x32_bf16 v[88:91], v[12:15], v[60:63], 0
	v_mfma_f32_16x16x32_bf16 v[68:71], v[8:11], v[40:43], v[68:71]
	v_mfma_f32_16x16x32_bf16 v[72:75], v[16:19], v[40:43], v[72:75]
	v_mfma_f32_16x16x32_bf16 v[76:79], v[8:11], v[48:51], v[76:79]
	v_mfma_f32_16x16x32_bf16 v[80:83], v[16:19], v[48:51], v[80:83]
	v_mfma_f32_16x16x32_bf16 v[84:87], v[8:11], v[56:59], v[84:87]
	v_mfma_f32_16x16x32_bf16 v[108:111], v[16:19], v[64:67], v[88:91]
	s_setprio 0
	s_setprio 1
	v_mfma_f32_16x16x32_bf16 v[88:91], v[20:23], v[36:39], 0
	v_mfma_f32_16x16x32_bf16 v[36:39], v[28:31], v[36:39], 0
	v_mfma_f32_16x16x32_bf16 v[112:115], v[24:27], v[40:43], v[88:91]
	v_mfma_f32_16x16x32_bf16 v[36:39], v[32:35], v[40:43], v[36:39]
	v_mfma_f32_16x16x32_bf16 v[40:43], v[20:23], v[44:47], 0
	v_mfma_f32_16x16x32_bf16 v[44:47], v[28:31], v[44:47], 0
	v_mfma_f32_16x16x32_bf16 v[40:43], v[24:27], v[48:51], v[40:43]
	v_mfma_f32_16x16x32_bf16 v[44:47], v[32:35], v[48:51], v[44:47]
	v_mfma_f32_16x16x32_bf16 v[48:51], v[20:23], v[52:55], 0
	v_mfma_f32_16x16x32_bf16 v[52:55], v[28:31], v[52:55], 0
	v_mfma_f32_16x16x32_bf16 v[48:51], v[24:27], v[56:59], v[48:51]
	v_mfma_f32_16x16x32_bf16 v[52:55], v[32:35], v[56:59], v[52:55]
	v_mfma_f32_16x16x32_bf16 v[56:59], v[20:23], v[60:63], 0
	v_mfma_f32_16x16x32_bf16 v[60:63], v[28:31], v[60:63], 0
	v_mfma_f32_16x16x32_bf16 v[56:59], v[24:27], v[64:67], v[56:59]
	v_mfma_f32_16x16x32_bf16 v[60:63], v[32:35], v[64:67], v[60:63]
	s_setprio 0
	s_barrier
	v_lshl_add_u64 v[214:215], s[12:13], 0, v[164:165]
	s_mov_b64 s[10:11], 0x100
	s_add_i32 s28, s28, s0
	v_lshl_add_u64 v[134:135], v[214:215], 0, s[10:11]
	s_mov_b32 m0, s28
	s_mov_b64 s[46:47], 0x40100
	s_add_i32 s29, s28, 0x2000
	ds_read_b128 v[64:67], v200 offset:16384
	ds_read_b128 v[88:91], v200 offset:17408
	ds_read_b128 v[100:103], v200 offset:18432
	ds_read_b128 v[104:107], v200 offset:19456
	ds_read_b128 v[116:119], v200 offset:20480
	ds_read_b128 v[120:123], v200 offset:21504
	ds_read_b128 v[124:127], v200 offset:22528
	ds_read_b128 v[128:131], v200 offset:23552
	global_load_lds_dwordx4 v[134:135], off
	v_lshl_add_u64 v[134:135], v[214:215], 0, s[46:47]
	s_mov_b32 m0, s29
	s_mov_b64 s[46:47], 0x80100
	s_add_i32 s33, s33, s0
	global_load_lds_dwordx4 v[134:135], off
	v_lshl_add_u64 v[134:135], v[214:215], 0, s[46:47]
	s_mov_b32 m0, s33
	s_mov_b64 s[46:47], 0xc0100
	s_add_i32 s45, s33, 0x2000
	global_load_lds_dwordx4 v[134:135], off
	v_lshl_add_u64 v[134:135], v[214:215], 0, s[46:47]
	s_mov_b32 m0, s45
	s_nop 0
	global_load_lds_dwordx4 v[134:135], off
	v_lshl_add_u64 v[134:135], v[194:195], 0, s[10:11]
	s_mov_b32 m0, s30
	s_mov_b64 s[10:11], 0x42100
	global_load_lds_dwordx4 v[134:135], off
	v_lshl_add_u64 v[134:135], v[194:195], 0, s[10:11]
	s_mov_b32 m0, s31
	s_nop 0
	global_load_lds_dwordx4 v[134:135], off
	s_waitcnt vmcnt(16)
	s_waitcnt lgkmcnt(0)
	s_barrier
	s_setprio 1
	s_waitcnt lgkmcnt(0)
	v_mfma_f32_16x16x32_bf16 v[134:137], v[4:7], v[64:67], 0
	v_mfma_f32_16x16x32_bf16 v[144:147], v[4:7], v[100:103], 0
	v_mfma_f32_16x16x32_bf16 v[152:155], v[4:7], v[116:119], 0
	v_mfma_f32_16x16x32_bf16 v[4:7], v[4:7], v[124:127], 0
	v_mfma_f32_16x16x32_bf16 v[136:139], v[8:11], v[88:91], v[134:137]
	v_mfma_f32_16x16x32_bf16 v[144:147], v[8:11], v[104:107], v[144:147]
	v_mfma_f32_16x16x32_bf16 v[152:155], v[8:11], v[120:123], v[152:155]
	v_mfma_f32_16x16x32_bf16 v[4:7], v[8:11], v[128:131], v[4:7]
	v_mfma_f32_16x16x32_bf16 v[8:11], v[12:15], v[124:127], 0
	v_mfma_f32_16x16x32_bf16 v[140:143], v[12:15], v[64:67], 0
	v_mfma_f32_16x16x32_bf16 v[148:151], v[12:15], v[100:103], 0
	v_mfma_f32_16x16x32_bf16 v[156:159], v[12:15], v[116:119], 0
	v_mfma_f32_16x16x32_bf16 v[12:15], v[16:19], v[128:131], v[8:11]
	v_mfma_f32_16x16x32_bf16 v[140:143], v[16:19], v[88:91], v[140:143]
	v_mfma_f32_16x16x32_bf16 v[148:151], v[16:19], v[104:107], v[148:151]
	v_mfma_f32_16x16x32_bf16 v[156:159], v[16:19], v[120:123], v[156:159]
	s_setprio 0
	s_setprio 1
	v_mfma_f32_16x16x32_bf16 v[8:11], v[20:23], v[64:67], 0
	v_mfma_f32_16x16x32_bf16 v[16:19], v[24:27], v[88:91], v[8:11]
	v_mfma_f32_16x16x32_bf16 v[8:11], v[28:31], v[64:67], 0
	v_mfma_f32_16x16x32_bf16 v[160:163], v[32:35], v[88:91], v[8:11]
	v_mfma_f32_16x16x32_bf16 v[8:11], v[20:23], v[100:103], 0
	v_mfma_f32_16x16x32_bf16 v[174:177], v[24:27], v[104:107], v[8:11]
	v_mfma_f32_16x16x32_bf16 v[8:11], v[28:31], v[100:103], 0
	v_mfma_f32_16x16x32_bf16 v[178:181], v[32:35], v[104:107], v[8:11]
	v_mfma_f32_16x16x32_bf16 v[8:11], v[20:23], v[116:119], 0
	v_mfma_f32_16x16x32_bf16 v[182:185], v[24:27], v[120:123], v[8:11]
	v_mfma_f32_16x16x32_bf16 v[8:11], v[28:31], v[116:119], 0
	v_mfma_f32_16x16x32_bf16 v[190:193], v[32:35], v[120:123], v[8:11]
	v_mfma_f32_16x16x32_bf16 v[8:11], v[20:23], v[124:127], 0
	v_mfma_f32_16x16x32_bf16 v[202:205], v[24:27], v[128:131], v[8:11]
	v_mfma_f32_16x16x32_bf16 v[8:11], v[28:31], v[124:127], 0
	v_mfma_f32_16x16x32_bf16 v[206:209], v[32:35], v[128:131], v[8:11]
	s_setprio 0
	s_barrier
	s_add_i32 s46, 0, 0x18000
	s_add_i32 s48, 0, 0x1c000
	v_add_u32_e32 v134, s46, v197
	v_add_u32_e32 v135, s48, v197
	s_nop 0
	ds_read_b128 v[8:11], v134
	ds_read_b128 v[28:31], v134 offset:1024
	ds_read_b128 v[32:35], v134 offset:2048
	ds_read_b128 v[64:67], v134 offset:3072
	ds_read_b128 v[216:219], v135
	ds_read_b128 v[220:223], v135 offset:1024
	ds_read_b128 v[224:227], v135 offset:2048
	ds_read_b128 v[228:231], v135 offset:3072
	s_mov_b64 s[10:11], 0x84100
	s_mov_b32 m0, s34
	v_lshl_add_u64 v[88:89], v[194:195], 0, s[10:11]
	s_mov_b64 s[10:11], 0xc6100
	ds_read_b128 v[20:23], v200 offset:32768
	ds_read_b128 v[24:27], v200 offset:33792
	ds_read_b128 v[232:235], v200 offset:34816
	ds_read_b128 v[236:239], v200 offset:35840
	ds_read_b128 v[240:243], v200 offset:36864
	ds_read_b128 v[244:247], v200 offset:37888
	ds_read_b128 v[248:251], v200 offset:38912
	ds_read_b128 v[186:189], v200 offset:39936
	global_load_lds_dwordx4 v[88:89], off
	v_lshl_add_u64 v[88:89], v[194:195], 0, s[10:11]
	s_mov_b32 m0, s35
	s_nop 0
	global_load_lds_dwordx4 v[88:89], off
	s_waitcnt vmcnt(8)
	s_waitcnt lgkmcnt(0)
	s_barrier
	s_setprio 1
	s_waitcnt lgkmcnt(0)
	v_mfma_f32_16x16x32_bf16 v[68:71], v[8:11], v[20:23], v[68:71]
	v_mfma_f32_16x16x32_bf16 v[120:123], v[28:31], v[24:27], v[68:71]
	v_mfma_f32_16x16x32_bf16 v[68:71], v[32:35], v[20:23], v[72:75]
	v_mfma_f32_16x16x32_bf16 v[116:119], v[64:67], v[24:27], v[68:71]
	v_mfma_f32_16x16x32_bf16 v[68:71], v[8:11], v[232:235], v[76:79]
	v_mfma_f32_16x16x32_bf16 v[104:107], v[28:31], v[236:239], v[68:71]
	v_mfma_f32_16x16x32_bf16 v[68:71], v[32:35], v[232:235], v[80:83]
	v_mfma_f32_16x16x32_bf16 v[100:103], v[64:67], v[236:239], v[68:71]
	v_mfma_f32_16x16x32_bf16 v[68:71], v[8:11], v[240:243], v[84:87]
	v_mfma_f32_16x16x32_bf16 v[88:91], v[28:31], v[244:247], v[68:71]
	v_mfma_f32_16x16x32_bf16 v[68:71], v[32:35], v[240:243], v[92:95]
	v_mfma_f32_16x16x32_bf16 v[84:87], v[64:67], v[244:247], v[68:71]
	v_mfma_f32_16x16x32_bf16 v[68:71], v[8:11], v[248:251], v[96:99]
	v_mfma_f32_16x16x32_bf16 v[72:75], v[28:31], v[186:189], v[68:71]
	v_mfma_f32_16x16x32_bf16 v[68:71], v[32:35], v[248:251], v[108:111]
	v_mfma_f32_16x16x32_bf16 v[68:71], v[64:67], v[186:189], v[68:71]
	s_setprio 0
	s_setprio 1
	v_mfma_f32_16x16x32_bf16 v[76:79], v[216:219], v[20:23], v[112:115]
	v_mfma_f32_16x16x32_bf16 v[20:23], v[224:227], v[20:23], v[36:39]
	v_mfma_f32_16x16x32_bf16 v[124:127], v[228:231], v[24:27], v[20:23]
	v_mfma_f32_16x16x32_bf16 v[20:23], v[216:219], v[232:235], v[40:43]
	v_mfma_f32_16x16x32_bf16 v[112:115], v[220:223], v[236:239], v[20:23]
	v_mfma_f32_16x16x32_bf16 v[20:23], v[224:227], v[232:235], v[44:47]
	v_mfma_f32_16x16x32_bf16 v[108:111], v[228:231], v[236:239], v[20:23]
	v_mfma_f32_16x16x32_bf16 v[20:23], v[216:219], v[240:243], v[48:51]
	v_mfma_f32_16x16x32_bf16 v[96:99], v[220:223], v[244:247], v[20:23]
	v_mfma_f32_16x16x32_bf16 v[20:23], v[224:227], v[240:243], v[52:55]
	v_mfma_f32_16x16x32_bf16 v[92:95], v[228:231], v[244:247], v[20:23]
	v_mfma_f32_16x16x32_bf16 v[20:23], v[216:219], v[248:251], v[56:59]
	v_mfma_f32_16x16x32_bf16 v[80:83], v[220:223], v[186:189], v[20:23]
	v_mfma_f32_16x16x32_bf16 v[20:23], v[224:227], v[248:251], v[60:63]
	v_mfma_f32_16x16x32_bf16 v[128:131], v[220:223], v[24:27], v[76:79]
	v_mfma_f32_16x16x32_bf16 v[76:79], v[228:231], v[186:189], v[20:23]
	s_setprio 0
	s_barrier
; #define PG8_MMA(ai, bj, At, Bt) do { __builtin_amdgcn_s_setprio(1); _Pragma("unroll") for (int m = 0; m < 4; ++m) _Pragma("unroll") for (int n = 0; n < 2; ++n) _Pragma("unroll") for (int k = 0; k < 2; ++k) \
;         acc[ai][bj][m][n] = __builtin_amdgcn_mfma_f32_16x16x32_bf16(Bt[n][k], At[m][k], acc[ai][bj][m][n], 0, 0, 0); __builtin_amdgcn_s_setprio(0); } while (0)
; #define PG8_WAIT_V(n) asm volatile("s_waitcnt vmcnt(" #n ")" ::: "memory")
; #define PG8_TRIP_HEAD(T) const int t = (T); const bool last = (t == nt - 2); \
;             const char* a1 = cA + (size_t)(t + 1) * kstep; \
;             const char* a2 = last ? nA : cA + (size_t)(t + 2) * kstep; const char* b2 = last ? nB : cB + (size_t)(t + 2) * kstep; \
;             const char* a3 = a2 + kstep; const char* b3 = b2 + kstep; \
;             if (last && has_next) S.a_ready(nxt);
; template <class Epi, class Sched, bool ALIGN_EPI = false, bool SP2 = false>
; __device__ __forceinline__ void gemm_phase(PG8_LAS unsigned char* lds, const Gemm g, const Sched& S, const Epi& E) {
;     ...
;         if constexpr (SP2) {
;             { PG8_TRIP_HEAD(0) PG8_TRIP_SP2(asm volatile("s_waitcnt vmcnt(%0)" :: "n"(8 + Epi::NST) : "memory"), PG8_MMAZ) }
;             for (int tt = 2; tt < nt; tt += 2) { PG8_TRIP_HEAD(tt) PG8_TRIP_SP2(PG8_WAIT_V(8), PG8_MMA) }
	s_mov_b64 s[10:11], 0x180
	s_add_i32 s46, s46, s0
	s_nop 1
	v_lshl_add_u64 v[20:21], v[214:215], 0, s[10:11]
	s_mov_b32 m0, s46
	s_mov_b64 s[50:51], 0x40180
	s_add_i32 s47, s46, 0x2000
	ds_read_b128 v[44:47], v200 offset:49152
	ds_read_b128 v[48:51], v200 offset:50176
	ds_read_b128 v[186:189], v200 offset:51200
	ds_read_b128 v[232:235], v200 offset:52224
	ds_read_b128 v[236:239], v200 offset:53248
	ds_read_b128 v[240:243], v200 offset:54272
	ds_read_b128 v[244:247], v200 offset:55296
	ds_read_b128 v[248:251], v200 offset:56320
	global_load_lds_dwordx4 v[20:21], off
	v_lshl_add_u64 v[20:21], v[214:215], 0, s[50:51]
	s_mov_b32 m0, s47
	s_mov_b64 s[50:51], 0x80180
	s_add_i32 s48, s48, s0
	global_load_lds_dwordx4 v[20:21], off
	v_lshl_add_u64 v[20:21], v[214:215], 0, s[50:51]
	s_mov_b32 m0, s48
	s_mov_b64 s[50:51], 0xc0180
	s_add_i32 s49, s48, 0x2000
	global_load_lds_dwordx4 v[20:21], off
	v_lshl_add_u64 v[20:21], v[214:215], 0, s[50:51]
	s_mov_b32 m0, s49
	s_nop 0
	global_load_lds_dwordx4 v[20:21], off
	v_lshl_add_u64 v[20:21], v[194:195], 0, s[10:11]
	s_mov_b32 m0, s38
	s_mov_b64 s[10:11], 0x42180
	global_load_lds_dwordx4 v[20:21], off
	v_lshl_add_u64 v[20:21], v[194:195], 0, s[10:11]
	s_mov_b32 m0, s39
	s_nop 0
	global_load_lds_dwordx4 v[20:21], off
	s_waitcnt vmcnt(8)
	s_waitcnt lgkmcnt(0)
	s_barrier
	s_setprio 1
	s_waitcnt lgkmcnt(0)
	v_mfma_f32_16x16x32_bf16 v[20:23], v[8:11], v[44:47], v[136:139]
	v_mfma_f32_16x16x32_bf16 v[56:59], v[28:31], v[48:51], v[20:23]
	v_mfma_f32_16x16x32_bf16 v[20:23], v[32:35], v[44:47], v[140:143]
	v_mfma_f32_16x16x32_bf16 v[52:55], v[64:67], v[48:51], v[20:23]
	v_mfma_f32_16x16x32_bf16 v[20:23], v[8:11], v[186:189], v[144:147]
	v_mfma_f32_16x16x32_bf16 v[40:43], v[28:31], v[232:235], v[20:23]
	v_mfma_f32_16x16x32_bf16 v[20:23], v[32:35], v[186:189], v[148:151]
	v_mfma_f32_16x16x32_bf16 v[36:39], v[64:67], v[232:235], v[20:23]
	v_mfma_f32_16x16x32_bf16 v[20:23], v[8:11], v[236:239], v[152:155]
	v_mfma_f32_16x16x32_bf16 v[4:7], v[8:11], v[244:247], v[4:7]
	v_mfma_f32_16x16x32_bf16 v[24:27], v[28:31], v[240:243], v[20:23]
	v_mfma_f32_16x16x32_bf16 v[20:23], v[32:35], v[236:239], v[156:159]
	v_mfma_f32_16x16x32_bf16 v[8:11], v[28:31], v[248:251], v[4:7]
	v_mfma_f32_16x16x32_bf16 v[4:7], v[32:35], v[244:247], v[12:15]
	v_mfma_f32_16x16x32_bf16 v[20:23], v[64:67], v[240:243], v[20:23]
	v_mfma_f32_16x16x32_bf16 v[4:7], v[64:67], v[248:251], v[4:7]
	s_setprio 0
	s_setprio 1
	v_mfma_f32_16x16x32_bf16 v[12:15], v[216:219], v[44:47], v[16:19]
	v_mfma_f32_16x16x32_bf16 v[64:67], v[220:223], v[48:51], v[12:15]
	v_mfma_f32_16x16x32_bf16 v[12:15], v[224:227], v[44:47], v[160:163]
	v_mfma_f32_16x16x32_bf16 v[60:63], v[228:231], v[48:51], v[12:15]
	v_mfma_f32_16x16x32_bf16 v[12:15], v[216:219], v[186:189], v[174:177]
	v_mfma_f32_16x16x32_bf16 v[48:51], v[220:223], v[232:235], v[12:15]
	v_mfma_f32_16x16x32_bf16 v[12:15], v[224:227], v[186:189], v[178:181]
	v_mfma_f32_16x16x32_bf16 v[44:47], v[228:231], v[232:235], v[12:15]
	v_mfma_f32_16x16x32_bf16 v[12:15], v[216:219], v[236:239], v[182:185]
	v_mfma_f32_16x16x32_bf16 v[32:35], v[220:223], v[240:243], v[12:15]
	v_mfma_f32_16x16x32_bf16 v[12:15], v[224:227], v[236:239], v[190:193]
	v_mfma_f32_16x16x32_bf16 v[28:31], v[228:231], v[240:243], v[12:15]
	v_mfma_f32_16x16x32_bf16 v[12:15], v[216:219], v[244:247], v[202:205]
	v_mfma_f32_16x16x32_bf16 v[16:19], v[220:223], v[248:251], v[12:15]
	v_mfma_f32_16x16x32_bf16 v[12:15], v[224:227], v[244:247], v[206:209]
	v_mfma_f32_16x16x32_bf16 v[12:15], v[228:231], v[248:251], v[12:15]
	s_setprio 0
	s_barrier
	s_add_u32 s10, s14, 0x84180
	s_addc_u32 s11, s15, 0
	s_add_u32 s12, s12, 0x200
	s_addc_u32 s13, s13, 0
	s_mov_b32 s14, 0
	s_mov_b64 s[54:55], 0x80000
	s_mov_b64 s[56:57], 0x80080
	s_mov_b64 s[60:61], 0xc0000
	s_mov_b64 s[62:63], 0xc0080
	s_mov_b64 s[64:65], 0xc6000

; #define PG8_BAR __builtin_amdgcn_s_barrier()
; template <class Epi, class Sched, bool ALIGN_EPI = false, bool SP2 = false>
; __device__ __forceinline__ void gemm_phase(PG8_LAS unsigned char* lds, const Gemm g, const Sched& S, const Epi& E) {
;     ...
;         if (!has_next) break;
;         if constexpr (!SP2) {
; #pragma unroll
;         for (int a = 0; a < 2; ++a)
; #pragma unroll
;             for (int b = 0; b < 2; ++b)
; #pragma unroll
;                 for (int m = 0; m < 4; ++m)
; #pragma unroll
;                     for (int n = 0; n < 2; ++n) acc[a][b][m][n] = (f32x4){0.f, 0.f, 0.f, 0.f};
;         }
;         cur = nxt; cA = nA; cB = nB; ++ui;
;         if constexpr (ALIGN_EPI) { if (wr == 1) PG8_BAR; }
.LBB0_364:
	s_andn2_b64 vcc, exec, s[16:17]
	s_cbranch_vccnz .LBB0_313
	s_mov_b32 s98, 1
	s_branch .LBB0_313

;     __device__ bool next(int i, Unit& u) const { const int rounds = nwg / G; if (i >= rounds) return false; return StaticOrder::next(rounds - 1 - i, u); }
;     __device__ bool next(int i, Unit& u) const { const int rounds = nwg / G; if (i >= 2 * rounds) return false; const bool ok = StaticOrder::next(i >= rounds ? i - rounds : i, u); u.z = (i >= rounds) ? 1 : 0; return ok; }
; template <class Epi, class Sched, bool ALIGN_EPI = false, bool SP2 = false>
; __device__ __forceinline__ void gemm_phase(PG8_LAS unsigned char* lds, const Gemm g, const Sched& S, const Epi& E) {
;     ...
;         const bool has_next = S.next(ui + 1, nxt);
;         const char* nA = has_next ? (const char*)S.opA(g, nxt) + (size_t)nxt.pm * tstepA : cA; const char* nB = has_next ? (const char*)S.opB(g, nxt) + (size_t)nxt.pn * tstepB : cB;
.LBB0_593:
	v_readlane_b32 s18, v253, 7
	v_readlane_b32 s34, v254, 59
	s_cmp_eq_u32 s29, 0
	v_readlane_b32 s19, v253, 8
	v_readlane_b32 s35, v254, 60
	s_cselect_b32 s33, s35, s19
	s_cselect_b32 s34, s34, s18
	s_ashr_i32 s15, s14, 31
	s_lshl_b64 s[18:19], s[14:15], 20
	s_add_u32 s18, s34, s18
	s_addc_u32 s19, s33, s19
	s_and_b64 s[4:5], s[4:5], exec
	s_cselect_b32 s4, s19, s9
	s_cselect_b32 s5, s18, s8
	s_cmp_eq_u32 s98, 1
	s_cbranch_scc0 .Llr_br
	s_barrier
	s_mov_b32 s98, 0
.Llr_br:
	s_add_i32 s35, 0, 0x10000
	s_add_i32 s37, 0, 0x14000
	v_add_u32_e32 v116, s35, v219
	v_add_u32_e32 v117, s37, v219
	ds_read_b128 v[4:7], v116
	ds_read_b128 v[8:11], v116 offset:1024
	ds_read_b128 v[12:15], v116 offset:2048
	ds_read_b128 v[16:19], v116 offset:3072
	ds_read_b128 v[20:23], v117
	ds_read_b128 v[24:27], v117 offset:1024
	ds_read_b128 v[28:31], v117 offset:2048
	ds_read_b128 v[32:35], v117 offset:3072
	s_mov_b32 s15, 0
	v_lshl_add_u64 v[192:193], s[20:21], 0, v[196:197]
	s_mov_b64 s[38:39], 0x84080
	s_add_i32 s33, s23, 0xc000
	v_lshl_add_u64 v[68:69], v[192:193], 0, s[38:39]
	s_mov_b32 m0, s33
	s_mov_b64 s[38:39], 0xc6080
	s_add_i32 s34, s23, 0xe000
	ds_read_b128 v[36:39], v221
	ds_read_b128 v[40:43], v221 offset:1024
	ds_read_b128 v[44:47], v221 offset:2048
	ds_read_b128 v[48:51], v221 offset:3072
	ds_read_b128 v[52:55], v221 offset:4096
	ds_read_b128 v[56:59], v221 offset:5120
	ds_read_b128 v[60:63], v221 offset:6144
	ds_read_b128 v[64:67], v221 offset:7168
	global_load_lds_dwordx4 v[68:69], off
	v_lshl_add_u64 v[68:69], v[192:193], 0, s[38:39]
	s_mov_b32 m0, s34
	s_nop 0
	global_load_lds_dwordx4 v[68:69], off
	s_waitcnt vmcnt(8)
	s_waitcnt lgkmcnt(0)
	s_barrier
	s_setprio 1
	s_waitcnt lgkmcnt(0)
	v_mfma_f32_16x16x32_bf16 v[92:95], v[4:7], v[60:63], 0
	v_mfma_f32_16x16x32_bf16 v[68:71], v[4:7], v[36:39], 0
	v_mfma_f32_16x16x32_bf16 v[72:75], v[12:15], v[36:39], 0
	v_mfma_f32_16x16x32_bf16 v[76:79], v[4:7], v[44:47], 0
	v_mfma_f32_16x16x32_bf16 v[80:83], v[12:15], v[44:47], 0
	v_mfma_f32_16x16x32_bf16 v[84:87], v[4:7], v[52:55], 0
	v_mfma_f32_16x16x32_bf16 v[88:91], v[12:15], v[52:55], 0
	v_mfma_f32_16x16x32_bf16 v[100:103], v[8:11], v[64:67], v[92:95]
	v_mfma_f32_16x16x32_bf16 v[92:95], v[12:15], v[60:63], 0
	v_mfma_f32_16x16x32_bf16 v[68:71], v[8:11], v[40:43], v[68:71]
	v_mfma_f32_16x16x32_bf16 v[72:75], v[16:19], v[40:43], v[72:75]
	v_mfma_f32_16x16x32_bf16 v[76:79], v[8:11], v[48:51], v[76:79]
	v_mfma_f32_16x16x32_bf16 v[80:83], v[16:19], v[48:51], v[80:83]
	v_mfma_f32_16x16x32_bf16 v[84:87], v[8:11], v[56:59], v[84:87]
	v_mfma_f32_16x16x32_bf16 v[88:91], v[16:19], v[56:59], v[88:91]
	v_mfma_f32_16x16x32_bf16 v[104:107], v[16:19], v[64:67], v[92:95]
	s_setprio 0
	s_setprio 1
	v_mfma_f32_16x16x32_bf16 v[92:95], v[20:23], v[36:39], 0
	v_mfma_f32_16x16x32_bf16 v[36:39], v[28:31], v[36:39], 0
	v_mfma_f32_16x16x32_bf16 v[118:121], v[24:27], v[40:43], v[92:95]
	v_mfma_f32_16x16x32_bf16 v[36:39], v[32:35], v[40:43], v[36:39]
	v_mfma_f32_16x16x32_bf16 v[40:43], v[20:23], v[44:47], 0
	v_mfma_f32_16x16x32_bf16 v[44:47], v[28:31], v[44:47], 0
	v_mfma_f32_16x16x32_bf16 v[40:43], v[24:27], v[48:51], v[40:43]
	v_mfma_f32_16x16x32_bf16 v[44:47], v[32:35], v[48:51], v[44:47]
	v_mfma_f32_16x16x32_bf16 v[48:51], v[20:23], v[52:55], 0
	v_mfma_f32_16x16x32_bf16 v[52:55], v[28:31], v[52:55], 0
	v_mfma_f32_16x16x32_bf16 v[48:51], v[24:27], v[56:59], v[48:51]
	v_mfma_f32_16x16x32_bf16 v[52:55], v[32:35], v[56:59], v[52:55]
	v_mfma_f32_16x16x32_bf16 v[56:59], v[20:23], v[60:63], 0
	v_mfma_f32_16x16x32_bf16 v[60:63], v[28:31], v[60:63], 0
	v_mfma_f32_16x16x32_bf16 v[56:59], v[24:27], v[64:67], v[56:59]
	v_mfma_f32_16x16x32_bf16 v[60:63], v[32:35], v[64:67], v[60:63]
	s_setprio 0
	s_barrier
	v_lshl_add_u64 v[250:251], s[8:9], 0, v[194:195]
	s_mov_b64 s[40:41], 0x100
	s_add_i32 s35, s35, s22
	v_lshl_add_u64 v[134:135], v[250:251], 0, s[40:41]
	s_mov_b32 m0, s35
	s_mov_b64 s[38:39], 0x40100
	s_add_i32 s36, s35, 0x2000
	ds_read_b128 v[64:67], v221 offset:16384
	ds_read_b128 v[92:95], v221 offset:17408
	ds_read_b128 v[96:99], v221 offset:18432
	ds_read_b128 v[108:111], v221 offset:19456
	ds_read_b128 v[112:115], v221 offset:20480
	ds_read_b128 v[122:125], v221 offset:21504
	ds_read_b128 v[126:129], v221 offset:22528
	ds_read_b128 v[130:133], v221 offset:23552
	global_load_lds_dwordx4 v[134:135], off
	v_lshl_add_u64 v[134:135], v[250:251], 0, s[38:39]
	s_mov_b32 m0, s36
	s_mov_b64 s[38:39], 0x80100
	s_add_i32 s37, s37, s22
	global_load_lds_dwordx4 v[134:135], off
	v_lshl_add_u64 v[134:135], v[250:251], 0, s[38:39]
	s_mov_b32 m0, s37
	s_mov_b64 s[38:39], 0xc0100
	global_load_lds_dwordx4 v[134:135], off
	v_lshl_add_u64 v[134:135], v[250:251], 0, s[38:39]
	s_add_i32 s38, s37, 0x2000
	s_mov_b32 m0, s38
	s_nop 0
	global_load_lds_dwordx4 v[134:135], off
	v_lshl_add_u64 v[134:135], v[192:193], 0, s[40:41]
	s_mov_b32 m0, s23
	s_mov_b64 s[40:41], 0x42100
	global_load_lds_dwordx4 v[134:135], off
	v_lshl_add_u64 v[134:135], v[192:193], 0, s[40:41]
	s_mov_b32 m0, s24
	s_nop 0
	global_load_lds_dwordx4 v[134:135], off
	s_waitcnt vmcnt(8)
	s_waitcnt lgkmcnt(0)
	s_barrier
	s_setprio 1
	s_waitcnt lgkmcnt(0)
	v_mfma_f32_16x16x32_bf16 v[134:137], v[4:7], v[64:67], 0
	v_mfma_f32_16x16x32_bf16 v[144:147], v[4:7], v[96:99], 0
	v_mfma_f32_16x16x32_bf16 v[152:155], v[4:7], v[112:115], 0
	v_mfma_f32_16x16x32_bf16 v[4:7], v[4:7], v[126:129], 0
	v_mfma_f32_16x16x32_bf16 v[136:139], v[8:11], v[92:95], v[134:137]
	v_mfma_f32_16x16x32_bf16 v[144:147], v[8:11], v[108:111], v[144:147]
	v_mfma_f32_16x16x32_bf16 v[152:155], v[8:11], v[122:125], v[152:155]
	v_mfma_f32_16x16x32_bf16 v[4:7], v[8:11], v[130:133], v[4:7]
	v_mfma_f32_16x16x32_bf16 v[8:11], v[12:15], v[126:129], 0
	v_mfma_f32_16x16x32_bf16 v[140:143], v[12:15], v[64:67], 0
	v_mfma_f32_16x16x32_bf16 v[148:151], v[12:15], v[96:99], 0
	v_mfma_f32_16x16x32_bf16 v[156:159], v[12:15], v[112:115], 0
	v_mfma_f32_16x16x32_bf16 v[8:11], v[16:19], v[130:133], v[8:11]
	v_mfma_f32_16x16x32_bf16 v[140:143], v[16:19], v[92:95], v[140:143]
	v_mfma_f32_16x16x32_bf16 v[148:151], v[16:19], v[108:111], v[148:151]
	v_mfma_f32_16x16x32_bf16 v[156:159], v[16:19], v[122:125], v[156:159]
	s_setprio 0
	s_setprio 1
	v_mfma_f32_16x16x32_bf16 v[12:15], v[20:23], v[64:67], 0
	v_mfma_f32_16x16x32_bf16 v[160:163], v[24:27], v[92:95], v[12:15]
	v_mfma_f32_16x16x32_bf16 v[12:15], v[28:31], v[64:67], 0
	v_mfma_f32_16x16x32_bf16 v[164:167], v[32:35], v[92:95], v[12:15]
	v_mfma_f32_16x16x32_bf16 v[12:15], v[20:23], v[96:99], 0
	v_mfma_f32_16x16x32_bf16 v[168:171], v[24:27], v[108:111], v[12:15]
	v_mfma_f32_16x16x32_bf16 v[12:15], v[28:31], v[96:99], 0
	v_mfma_f32_16x16x32_bf16 v[172:175], v[32:35], v[108:111], v[12:15]
	v_mfma_f32_16x16x32_bf16 v[12:15], v[20:23], v[112:115], 0
	v_mfma_f32_16x16x32_bf16 v[176:179], v[24:27], v[122:125], v[12:15]
	v_mfma_f32_16x16x32_bf16 v[12:15], v[28:31], v[112:115], 0
	v_mfma_f32_16x16x32_bf16 v[180:183], v[32:35], v[122:125], v[12:15]
	v_mfma_f32_16x16x32_bf16 v[12:15], v[20:23], v[126:129], 0
	v_mfma_f32_16x16x32_bf16 v[184:187], v[24:27], v[130:133], v[12:15]
	v_mfma_f32_16x16x32_bf16 v[12:15], v[28:31], v[126:129], 0
	v_mfma_f32_16x16x32_bf16 v[188:191], v[32:35], v[130:133], v[12:15]
	s_setprio 0
	s_barrier
	s_add_i32 s39, 0, 0x18000
	s_add_i32 s41, 0, 0x1c000
	v_add_u32_e32 v134, s39, v219
	v_add_u32_e32 v135, s41, v219
	s_nop 0
	ds_read_b128 v[12:15], v134
	ds_read_b128 v[16:19], v134 offset:1024
	ds_read_b128 v[20:23], v134 offset:2048
	ds_read_b128 v[24:27], v134 offset:3072
	ds_read_b128 v[202:205], v135
	ds_read_b128 v[206:209], v135 offset:1024
	ds_read_b128 v[222:225], v135 offset:2048
	ds_read_b128 v[226:229], v135 offset:3072
	s_mov_b64 s[42:43], 0x84100
	s_mov_b32 m0, s25
	v_lshl_add_u64 v[92:93], v[192:193], 0, s[42:43]
	s_mov_b64 s[42:43], 0xc6100
	ds_read_b128 v[28:31], v221 offset:32768
	ds_read_b128 v[32:35], v221 offset:33792
	ds_read_b128 v[64:67], v221 offset:34816
	ds_read_b128 v[230:233], v221 offset:35840
	ds_read_b128 v[234:237], v221 offset:36864
	ds_read_b128 v[238:241], v221 offset:37888
	ds_read_b128 v[242:245], v221 offset:38912
	ds_read_b128 v[246:249], v221 offset:39936
	global_load_lds_dwordx4 v[92:93], off
	v_lshl_add_u64 v[92:93], v[192:193], 0, s[42:43]
	s_mov_b32 m0, s26
	s_nop 0
	global_load_lds_dwordx4 v[92:93], off
	s_waitcnt vmcnt(8)
	s_waitcnt lgkmcnt(0)
	s_barrier
	s_setprio 1
	s_waitcnt lgkmcnt(0)
	v_mfma_f32_16x16x32_bf16 v[68:71], v[12:15], v[28:31], v[68:71]
	v_mfma_f32_16x16x32_bf16 v[130:133], v[16:19], v[32:35], v[68:71]
	v_mfma_f32_16x16x32_bf16 v[68:71], v[20:23], v[28:31], v[72:75]
	v_mfma_f32_16x16x32_bf16 v[126:129], v[24:27], v[32:35], v[68:71]
	v_mfma_f32_16x16x32_bf16 v[68:71], v[12:15], v[64:67], v[76:79]
	v_mfma_f32_16x16x32_bf16 v[112:115], v[16:19], v[230:233], v[68:71]
	v_mfma_f32_16x16x32_bf16 v[68:71], v[20:23], v[64:67], v[80:83]
	v_mfma_f32_16x16x32_bf16 v[108:111], v[24:27], v[230:233], v[68:71]
	v_mfma_f32_16x16x32_bf16 v[68:71], v[12:15], v[234:237], v[84:87]
	v_mfma_f32_16x16x32_bf16 v[96:99], v[16:19], v[238:241], v[68:71]
	v_mfma_f32_16x16x32_bf16 v[68:71], v[20:23], v[234:237], v[88:91]
	v_mfma_f32_16x16x32_bf16 v[92:95], v[24:27], v[238:241], v[68:71]
	v_mfma_f32_16x16x32_bf16 v[68:71], v[12:15], v[242:245], v[100:103]
	v_mfma_f32_16x16x32_bf16 v[80:83], v[16:19], v[246:249], v[68:71]
	v_mfma_f32_16x16x32_bf16 v[68:71], v[20:23], v[242:245], v[104:107]
	v_mfma_f32_16x16x32_bf16 v[76:79], v[24:27], v[246:249], v[68:71]
	s_setprio 0
	s_setprio 1
	v_mfma_f32_16x16x32_bf16 v[68:71], v[202:205], v[28:31], v[118:121]
	v_mfma_f32_16x16x32_bf16 v[28:31], v[222:225], v[28:31], v[36:39]
	v_mfma_f32_16x16x32_bf16 v[118:121], v[226:229], v[32:35], v[28:31]
	v_mfma_f32_16x16x32_bf16 v[28:31], v[202:205], v[64:67], v[40:43]
	v_mfma_f32_16x16x32_bf16 v[104:107], v[206:209], v[230:233], v[28:31]
	v_mfma_f32_16x16x32_bf16 v[28:31], v[222:225], v[64:67], v[44:47]
	v_mfma_f32_16x16x32_bf16 v[100:103], v[226:229], v[230:233], v[28:31]
	v_mfma_f32_16x16x32_bf16 v[28:31], v[202:205], v[234:237], v[48:51]
	v_mfma_f32_16x16x32_bf16 v[88:91], v[206:209], v[238:241], v[28:31]
	v_mfma_f32_16x16x32_bf16 v[28:31], v[222:225], v[234:237], v[52:55]
	v_mfma_f32_16x16x32_bf16 v[84:87], v[226:229], v[238:241], v[28:31]
	v_mfma_f32_16x16x32_bf16 v[28:31], v[202:205], v[242:245], v[56:59]
	v_mfma_f32_16x16x32_bf16 v[72:75], v[206:209], v[246:249], v[28:31]
	v_mfma_f32_16x16x32_bf16 v[28:31], v[222:225], v[242:245], v[60:63]
	v_mfma_f32_16x16x32_bf16 v[122:125], v[206:209], v[32:35], v[68:71]
	v_mfma_f32_16x16x32_bf16 v[68:71], v[226:229], v[246:249], v[28:31]
	s_setprio 0
	s_barrier
; #define PG8_MMA(ai, bj, At, Bt) do { __builtin_amdgcn_s_setprio(1); _Pragma("unroll") for (int m = 0; m < 4; ++m) _Pragma("unroll") for (int n = 0; n < 2; ++n) _Pragma("unroll") for (int k = 0; k < 2; ++k) \
;         acc[ai][bj][m][n] = __builtin_amdgcn_mfma_f32_16x16x32_bf16(Bt[n][k], At[m][k], acc[ai][bj][m][n], 0, 0, 0); __builtin_amdgcn_s_setprio(0); } while (0)
; #define PG8_WAIT_V(n) asm volatile("s_waitcnt vmcnt(" #n ")" ::: "memory")
; #define PG8_TRIP_HEAD(T) const int t = (T); const bool last = (t == nt - 2); \
;             const char* a1 = cA + (size_t)(t + 1) * kstep; \
;             const char* a2 = last ? nA : cA + (size_t)(t + 2) * kstep; const char* b2 = last ? nB : cB + (size_t)(t + 2) * kstep; \
;             const char* a3 = a2 + kstep; const char* b3 = b2 + kstep; \
;             if (last && has_next) S.a_ready(nxt);
; template <class Epi, class Sched, bool ALIGN_EPI = false, bool SP2 = false>
; __device__ __forceinline__ void gemm_phase(PG8_LAS unsigned char* lds, const Gemm g, const Sched& S, const Epi& E) {
;     ...
;         if constexpr (SP2) {
;             { PG8_TRIP_HEAD(0) PG8_TRIP_SP2(asm volatile("s_waitcnt vmcnt(%0)" :: "n"(8 + Epi::NST) : "memory"), PG8_MMAZ) }
;             for (int tt = 2; tt < nt; tt += 2) { PG8_TRIP_HEAD(tt) PG8_TRIP_SP2(PG8_WAIT_V(8), PG8_MMA) }
	s_mov_b64 s[44:45], 0x180
	s_add_i32 s39, s39, s22
	s_nop 1
	v_lshl_add_u64 v[28:29], v[250:251], 0, s[44:45]
	s_mov_b32 m0, s39
	s_mov_b64 s[42:43], 0x40180
	s_add_i32 s40, s39, 0x2000
	ds_read_b128 v[36:39], v221 offset:49152
	ds_read_b128 v[40:43], v221 offset:50176
	ds_read_b128 v[230:233], v221 offset:51200
	ds_read_b128 v[234:237], v221 offset:52224
	ds_read_b128 v[238:241], v221 offset:53248
	ds_read_b128 v[242:245], v221 offset:54272
	ds_read_b128 v[246:249], v221 offset:55296
	ds_read_b128 v[214:217], v221 offset:56320
	global_load_lds_dwordx4 v[28:29], off
	v_lshl_add_u64 v[28:29], v[250:251], 0, s[42:43]
	s_mov_b32 m0, s40
	s_mov_b64 s[42:43], 0x80180
	s_add_i32 s41, s41, s22
	global_load_lds_dwordx4 v[28:29], off
	v_lshl_add_u64 v[28:29], v[250:251], 0, s[42:43]
	s_mov_b32 m0, s41
	s_mov_b64 s[42:43], 0xc0180
	global_load_lds_dwordx4 v[28:29], off
	v_lshl_add_u64 v[28:29], v[250:251], 0, s[42:43]
	s_add_i32 s42, s41, 0x2000
	s_mov_b32 m0, s42
	s_nop 0
	global_load_lds_dwordx4 v[28:29], off
	v_lshl_add_u64 v[28:29], v[192:193], 0, s[44:45]
	s_mov_b32 m0, s27
	s_mov_b64 s[44:45], 0x42180
	global_load_lds_dwordx4 v[28:29], off
	v_lshl_add_u64 v[28:29], v[192:193], 0, s[44:45]
	s_mov_b32 m0, s28
	s_nop 0
	global_load_lds_dwordx4 v[28:29], off
	s_waitcnt vmcnt(8)
	s_waitcnt lgkmcnt(0)
	s_barrier
	s_setprio 1
	s_waitcnt lgkmcnt(0)
	v_mfma_f32_16x16x32_bf16 v[28:31], v[12:15], v[36:39], v[136:139]
	v_mfma_f32_16x16x32_bf16 v[64:67], v[16:19], v[40:43], v[28:31]
	v_mfma_f32_16x16x32_bf16 v[28:31], v[20:23], v[36:39], v[140:143]
	v_mfma_f32_16x16x32_bf16 v[60:63], v[24:27], v[40:43], v[28:31]
	v_mfma_f32_16x16x32_bf16 v[28:31], v[12:15], v[230:233], v[144:147]
	v_mfma_f32_16x16x32_bf16 v[48:51], v[16:19], v[234:237], v[28:31]
	v_mfma_f32_16x16x32_bf16 v[28:31], v[20:23], v[230:233], v[148:151]
	v_mfma_f32_16x16x32_bf16 v[44:47], v[24:27], v[234:237], v[28:31]
	v_mfma_f32_16x16x32_bf16 v[28:31], v[12:15], v[238:241], v[152:155]
	v_mfma_f32_16x16x32_bf16 v[4:7], v[12:15], v[246:249], v[4:7]
	v_mfma_f32_16x16x32_bf16 v[32:35], v[16:19], v[242:245], v[28:31]
	v_mfma_f32_16x16x32_bf16 v[28:31], v[20:23], v[238:241], v[156:159]
	v_mfma_f32_16x16x32_bf16 v[16:19], v[16:19], v[214:217], v[4:7]
	v_mfma_f32_16x16x32_bf16 v[4:7], v[20:23], v[246:249], v[8:11]
	v_mfma_f32_16x16x32_bf16 v[28:31], v[24:27], v[242:245], v[28:31]
	v_mfma_f32_16x16x32_bf16 v[12:15], v[24:27], v[214:217], v[4:7]
	s_setprio 0
	s_setprio 1
	v_mfma_f32_16x16x32_bf16 v[4:7], v[202:205], v[36:39], v[160:163]
	v_mfma_f32_16x16x32_bf16 v[56:59], v[206:209], v[40:43], v[4:7]
	v_mfma_f32_16x16x32_bf16 v[4:7], v[222:225], v[36:39], v[164:167]
	v_mfma_f32_16x16x32_bf16 v[52:55], v[226:229], v[40:43], v[4:7]
	v_mfma_f32_16x16x32_bf16 v[4:7], v[202:205], v[230:233], v[168:171]
	v_mfma_f32_16x16x32_bf16 v[40:43], v[206:209], v[234:237], v[4:7]
	v_mfma_f32_16x16x32_bf16 v[4:7], v[222:225], v[230:233], v[172:175]
	v_mfma_f32_16x16x32_bf16 v[36:39], v[226:229], v[234:237], v[4:7]
	v_mfma_f32_16x16x32_bf16 v[4:7], v[202:205], v[238:241], v[176:179]
	v_mfma_f32_16x16x32_bf16 v[24:27], v[206:209], v[242:245], v[4:7]
	v_mfma_f32_16x16x32_bf16 v[4:7], v[222:225], v[238:241], v[180:183]
	v_mfma_f32_16x16x32_bf16 v[20:23], v[226:229], v[242:245], v[4:7]
	v_mfma_f32_16x16x32_bf16 v[4:7], v[202:205], v[246:249], v[184:187]
	v_mfma_f32_16x16x32_bf16 v[8:11], v[206:209], v[214:217], v[4:7]
	v_mfma_f32_16x16x32_bf16 v[4:7], v[222:225], v[246:249], v[188:191]
	v_mfma_f32_16x16x32_bf16 v[4:7], v[226:229], v[214:217], v[4:7]
	s_setprio 0
	s_barrier
	s_add_u32 s20, s20, 0x84180
	s_addc_u32 s21, s21, 0
	s_add_u32 s8, s8, 0x200
	s_addc_u32 s9, s9, 0
	s_mov_b64 s[48:49], 0x80000
	s_mov_b64 s[50:51], 0x80080
	s_mov_b64 s[52:53], 0xc0000
	s_mov_b64 s[54:55], 0xc0080
	s_mov_b64 s[56:57], 0xc6000

; __device__ __forceinline__ unsigned cvt_pk_bf16(float lo, float hi) { f32x2_c v = {lo, hi}; bf16x2_c b = __builtin_convertvector(v, bf16x2_c); return __builtin_bit_cast(unsigned, b); }
; __device__ __forceinline__ float bf_lo(unsigned u) { return __uint_as_float(u << 16); }
; __device__ __forceinline__ float bf_hi(unsigned u) { return __uint_as_float(u & 0xffff0000u); }
;     __device__ __forceinline__ void operator()(const f32x4 (&acc)[2][2][4][2], const Unit& u, int wr, int wc, int fr, int fq) const {
;     ...
;             for (int m = 0; m < 4; ++m)
; #pragma unroll
;                 for (int bj = 0; bj < 2; ++bj) { const size_t off = (size_t)(row0 + ai * HALF + m * 16) * LDT + col0 + bj * HALF; const unsigned g0 = bj ? gv[m].z : gv[m].x, g1 = bj ? gv[m].w : gv[m].y;
;                     const f32x4 a0 = acc[ai][bj][m][0] * (1.0f / 255.0f), a1 = acc[ai][bj][m][1] * (1.0f / 255.0f);
;                     float o[8] = {a0[0] * (float)(g0 & 255u), a0[1] * (float)((g0 >> 8) & 255u), a0[2] * (float)((g0 >> 16) & 255u), a0[3] * (float)(g0 >> 24), a1[0] * (float)(g1 & 255u), a1[1] * (float)((g1 >> 8) & 255u), a1[2] * (float)((g1 >> 16) & 255u), a1[3] * (float)(g1 >> 24)};
;                     { const u32x4 pw = pv[m][bj];
;                         o[0] += bf_lo(pw.x); o[1] += bf_hi(pw.x); o[2] += bf_lo(pw.y); o[3] += bf_hi(pw.y); o[4] += bf_lo(pw.z); o[5] += bf_hi(pw.z); o[6] += bf_lo(pw.w); o[7] += bf_hi(pw.w); }
;                     u32x4 w; w.x = cvt_pk_bf16(o[0], o[1]); w.y = cvt_pk_bf16(o[2], o[3]); w.z = cvt_pk_bf16(o[4], o[5]); w.w = cvt_pk_bf16(o[6], o[7]);
;                     *(u32x4*)(T + off) = w; }
.LBB0_629:
	s_mov_b32 s0, 0x3b808081
	v_pk_mul_f32 v[64:65], v[64:65], s[0:1] op_sel_hi:[1,0]
	s_waitcnt vmcnt(3)
	v_cvt_f32_ubyte1_e32 v113, v104
	v_cvt_f32_ubyte0_e32 v112, v104
	v_lshlrev_b32_e32 v122, 16, v116
	v_and_b32_e32 v123, 0xffff0000, v116
	v_pk_mul_f32 v[66:67], v[66:67], s[0:1] op_sel_hi:[1,0]
	v_pk_fma_f32 v[64:65], v[64:65], v[112:113], v[122:123]
	v_cvt_f32_ubyte3_e32 v113, v104
	v_cvt_f32_ubyte2_e32 v112, v104
	v_lshlrev_b32_e32 v116, 16, v117
	v_and_b32_e32 v117, 0xffff0000, v117
	v_pk_mul_f32 v[60:61], v[60:61], s[0:1] op_sel_hi:[1,0]
	v_pk_fma_f32 v[66:67], v[66:67], v[112:113], v[116:117]
	v_cvt_f32_ubyte1_e32 v113, v105
	v_cvt_f32_ubyte0_e32 v112, v105
	v_lshlrev_b32_e32 v116, 16, v118
	v_and_b32_e32 v117, 0xffff0000, v118
	v_pk_mul_f32 v[62:63], v[62:63], s[0:1] op_sel_hi:[1,0]
	v_pk_fma_f32 v[60:61], v[60:61], v[112:113], v[116:117]
	v_cvt_f32_ubyte3_e32 v113, v105
	v_cvt_f32_ubyte2_e32 v112, v105
	v_lshlrev_b32_e32 v104, 16, v119
	v_and_b32_e32 v105, 0xffff0000, v119
	v_pk_fma_f32 v[104:105], v[62:63], v[112:113], v[104:105]
	v_cvt_pk_bf16_f32 v62, v64, v65
	v_cvt_pk_bf16_f32 v64, v60, v61
	v_mov_b64_e32 v[60:61], s[94:95]
	v_cvt_pk_bf16_f32 v63, v66, v67
	v_mad_i64_i32 v[66:67], s[4:5], v121, s81, v[60:61]
	v_cvt_pk_bf16_f32 v65, v104, v105
	v_lshl_add_u64 v[66:67], v[66:67], 0, v[126:127]
	global_store_dwordx4 v[66:67], v[62:65], off
	v_pk_mul_f32 v[56:57], v[56:57], s[0:1] op_sel_hi:[1,0]
	v_pk_mul_f32 v[58:59], v[58:59], s[0:1] op_sel_hi:[1,0]
	v_cvt_f32_ubyte1_e32 v63, v106
	v_cvt_f32_ubyte0_e32 v62, v106
	v_lshlrev_b32_e32 v64, 16, v108
	v_and_b32_e32 v65, 0xffff0000, v108
	v_pk_fma_f32 v[56:57], v[56:57], v[62:63], v[64:65]
	v_cvt_f32_ubyte3_e32 v63, v106
	v_cvt_f32_ubyte2_e32 v62, v106
	v_lshlrev_b32_e32 v64, 16, v109
	v_and_b32_e32 v65, 0xffff0000, v109
	v_pk_mul_f32 v[52:53], v[52:53], s[0:1] op_sel_hi:[1,0]
	v_pk_fma_f32 v[58:59], v[58:59], v[62:63], v[64:65]
	v_cvt_f32_ubyte1_e32 v63, v107
	v_cvt_f32_ubyte0_e32 v62, v107
	v_lshlrev_b32_e32 v64, 16, v110
	v_and_b32_e32 v65, 0xffff0000, v110
	v_pk_mul_f32 v[54:55], v[54:55], s[0:1] op_sel_hi:[1,0]
	v_pk_fma_f32 v[62:63], v[52:53], v[62:63], v[64:65]
	v_cvt_f32_ubyte3_e32 v53, v107
	v_cvt_f32_ubyte2_e32 v52, v107
	v_lshlrev_b32_e32 v64, 16, v111
	v_and_b32_e32 v65, 0xffff0000, v111
	v_pk_fma_f32 v[64:65], v[54:55], v[52:53], v[64:65]
	v_cvt_pk_bf16_f32 v52, v56, v57
	v_cvt_pk_bf16_f32 v53, v58, v59
	v_cvt_pk_bf16_f32 v54, v62, v63
	v_cvt_pk_bf16_f32 v55, v64, v65
	global_store_dwordx4 v[66:67], v[52:55], off offset:256
	v_pk_mul_f32 v[48:49], v[48:49], s[0:1] op_sel_hi:[1,0]
	v_pk_mul_f32 v[50:51], v[50:51], s[0:1] op_sel_hi:[1,0]
	s_waitcnt vmcnt(4)
	v_cvt_f32_ubyte1_e32 v53, v92
	v_cvt_f32_ubyte0_e32 v52, v92
	v_lshlrev_b32_e32 v54, 16, v96
	v_and_b32_e32 v55, 0xffff0000, v96
	v_pk_fma_f32 v[48:49], v[48:49], v[52:53], v[54:55]
	v_cvt_f32_ubyte3_e32 v53, v92
	v_cvt_f32_ubyte2_e32 v52, v92
	v_lshlrev_b32_e32 v54, 16, v97
	v_and_b32_e32 v55, 0xffff0000, v97
	v_pk_mul_f32 v[44:45], v[44:45], s[0:1] op_sel_hi:[1,0]
	v_pk_fma_f32 v[50:51], v[50:51], v[52:53], v[54:55]
	v_cvt_f32_ubyte1_e32 v53, v93
	v_cvt_f32_ubyte0_e32 v52, v93
	v_lshlrev_b32_e32 v54, 16, v98
	v_and_b32_e32 v55, 0xffff0000, v98
	v_pk_mul_f32 v[46:47], v[46:47], s[0:1] op_sel_hi:[1,0]
	v_pk_fma_f32 v[52:53], v[44:45], v[52:53], v[54:55]
	v_cvt_f32_ubyte3_e32 v45, v93
	v_cvt_f32_ubyte2_e32 v44, v93
	v_lshlrev_b32_e32 v54, 16, v99
	v_and_b32_e32 v55, 0xffff0000, v99
	v_pk_fma_f32 v[54:55], v[46:47], v[44:45], v[54:55]
	v_cvt_pk_bf16_f32 v44, v48, v49
	v_mad_i64_i32 v[48:49], s[4:5], v120, s81, v[60:61]
	v_cvt_pk_bf16_f32 v45, v50, v51
	v_cvt_pk_bf16_f32 v46, v52, v53
	v_cvt_pk_bf16_f32 v47, v54, v55
	v_lshl_add_u64 v[48:49], v[48:49], 0, v[126:127]
	global_store_dwordx4 v[48:49], v[44:47], off
	v_pk_mul_f32 v[40:41], v[40:41], s[0:1] op_sel_hi:[1,0]
	v_pk_mul_f32 v[42:43], v[42:43], s[0:1] op_sel_hi:[1,0]
	v_cvt_f32_ubyte1_e32 v45, v94
	v_cvt_f32_ubyte0_e32 v44, v94
	v_lshlrev_b32_e32 v46, 16, v100
	v_and_b32_e32 v47, 0xffff0000, v100
	v_pk_fma_f32 v[40:41], v[40:41], v[44:45], v[46:47]
	v_cvt_f32_ubyte3_e32 v45, v94
	v_cvt_f32_ubyte2_e32 v44, v94
	v_lshlrev_b32_e32 v46, 16, v101
	v_and_b32_e32 v47, 0xffff0000, v101
	v_pk_mul_f32 v[36:37], v[36:37], s[0:1] op_sel_hi:[1,0]
	v_pk_fma_f32 v[42:43], v[42:43], v[44:45], v[46:47]
	v_cvt_f32_ubyte1_e32 v45, v95
	v_cvt_f32_ubyte0_e32 v44, v95
	v_lshlrev_b32_e32 v46, 16, v102
	v_and_b32_e32 v47, 0xffff0000, v102
	v_pk_mul_f32 v[38:39], v[38:39], s[0:1] op_sel_hi:[1,0]
	v_pk_fma_f32 v[44:45], v[36:37], v[44:45], v[46:47]
	v_cvt_f32_ubyte3_e32 v37, v95
	v_cvt_f32_ubyte2_e32 v36, v95
	v_lshlrev_b32_e32 v46, 16, v103
	v_and_b32_e32 v47, 0xffff0000, v103
	v_pk_fma_f32 v[46:47], v[38:39], v[36:37], v[46:47]
	v_cvt_pk_bf16_f32 v36, v40, v41
	v_cvt_pk_bf16_f32 v37, v42, v43
	v_cvt_pk_bf16_f32 v38, v44, v45
	v_cvt_pk_bf16_f32 v39, v46, v47
	global_store_dwordx4 v[48:49], v[36:39], off offset:256
	v_pk_mul_f32 v[32:33], v[32:33], s[0:1] op_sel_hi:[1,0]
	v_pk_mul_f32 v[34:35], v[34:35], s[0:1] op_sel_hi:[1,0]
	s_waitcnt vmcnt(5)
; __device__ __forceinline__ unsigned cvt_pk_bf16(float lo, float hi) { f32x2_c v = {lo, hi}; bf16x2_c b = __builtin_convertvector(v, bf16x2_c); return __builtin_bit_cast(unsigned, b); }
; __device__ __forceinline__ float bf_lo(unsigned u) { return __uint_as_float(u << 16); }
; __device__ __forceinline__ float bf_hi(unsigned u) { return __uint_as_float(u & 0xffff0000u); }
; #define PG8_BAR __builtin_amdgcn_s_barrier()
;     __device__ __forceinline__ void operator()(const f32x4 (&acc)[2][2][4][2], const Unit& u, int wr, int wc, int fr, int fq) const {
;     ...
;             for (int m = 0; m < 4; ++m)
; #pragma unroll
;                 for (int bj = 0; bj < 2; ++bj) { const size_t off = (size_t)(row0 + ai * HALF + m * 16) * LDT + col0 + bj * HALF; const unsigned g0 = bj ? gv[m].z : gv[m].x, g1 = bj ? gv[m].w : gv[m].y;
;                     const f32x4 a0 = acc[ai][bj][m][0] * (1.0f / 255.0f), a1 = acc[ai][bj][m][1] * (1.0f / 255.0f);
;                     float o[8] = {a0[0] * (float)(g0 & 255u), a0[1] * (float)((g0 >> 8) & 255u), a0[2] * (float)((g0 >> 16) & 255u), a0[3] * (float)(g0 >> 24), a1[0] * (float)(g1 & 255u), a1[1] * (float)((g1 >> 8) & 255u), a1[2] * (float)((g1 >> 16) & 255u), a1[3] * (float)(g1 >> 24)};
;                     { const u32x4 pw = pv[m][bj];
;                         o[0] += bf_lo(pw.x); o[1] += bf_hi(pw.x); o[2] += bf_lo(pw.y); o[3] += bf_hi(pw.y); o[4] += bf_lo(pw.z); o[5] += bf_hi(pw.z); o[6] += bf_lo(pw.w); o[7] += bf_hi(pw.w); }
;                     u32x4 w; w.x = cvt_pk_bf16(o[0], o[1]); w.y = cvt_pk_bf16(o[2], o[3]); w.z = cvt_pk_bf16(o[4], o[5]); w.w = cvt_pk_bf16(o[6], o[7]);
;                     *(u32x4*)(T + off) = w; }
; template <class Epi, class Sched, bool ALIGN_EPI = false, bool SP2 = false>
; __device__ __forceinline__ void gemm_phase(PG8_LAS unsigned char* lds, const Gemm g, const Sched& S, const Epi& E) {
;     ...
;         cur = nxt; cA = nA; cB = nB; ++ui;
;         if constexpr (ALIGN_EPI) { if (wr == 1) PG8_BAR; }
	v_cvt_f32_ubyte1_e32 v37, v80
	v_cvt_f32_ubyte0_e32 v36, v80
	v_lshlrev_b32_e32 v38, 16, v84
	v_and_b32_e32 v39, 0xffff0000, v84
	v_pk_fma_f32 v[32:33], v[32:33], v[36:37], v[38:39]
	v_cvt_f32_ubyte3_e32 v37, v80
	v_cvt_f32_ubyte2_e32 v36, v80
	v_lshlrev_b32_e32 v38, 16, v85
	v_and_b32_e32 v39, 0xffff0000, v85
	v_pk_mul_f32 v[28:29], v[28:29], s[0:1] op_sel_hi:[1,0]
	v_pk_fma_f32 v[34:35], v[34:35], v[36:37], v[38:39]
	v_cvt_f32_ubyte1_e32 v37, v81
	v_cvt_f32_ubyte0_e32 v36, v81
	v_lshlrev_b32_e32 v38, 16, v86
	v_and_b32_e32 v39, 0xffff0000, v86
	v_pk_mul_f32 v[30:31], v[30:31], s[0:1] op_sel_hi:[1,0]
	v_pk_fma_f32 v[36:37], v[28:29], v[36:37], v[38:39]
	v_cvt_f32_ubyte3_e32 v29, v81
	v_cvt_f32_ubyte2_e32 v28, v81
	v_lshlrev_b32_e32 v38, 16, v87
	v_and_b32_e32 v39, 0xffff0000, v87
	v_pk_fma_f32 v[38:39], v[30:31], v[28:29], v[38:39]
	v_cvt_pk_bf16_f32 v28, v32, v33
	v_mad_i64_i32 v[32:33], s[4:5], v115, s81, v[60:61]
	v_cvt_pk_bf16_f32 v29, v34, v35
	v_cvt_pk_bf16_f32 v30, v36, v37
	v_cvt_pk_bf16_f32 v31, v38, v39
	v_lshl_add_u64 v[32:33], v[32:33], 0, v[126:127]
	global_store_dwordx4 v[32:33], v[28:31], off
	v_pk_mul_f32 v[24:25], v[24:25], s[0:1] op_sel_hi:[1,0]
	v_pk_mul_f32 v[26:27], v[26:27], s[0:1] op_sel_hi:[1,0]
	v_cvt_f32_ubyte1_e32 v29, v82
	v_cvt_f32_ubyte0_e32 v28, v82
	v_lshlrev_b32_e32 v30, 16, v88
	v_and_b32_e32 v31, 0xffff0000, v88
	v_pk_fma_f32 v[24:25], v[24:25], v[28:29], v[30:31]
	v_cvt_f32_ubyte3_e32 v29, v82
	v_cvt_f32_ubyte2_e32 v28, v82
	v_lshlrev_b32_e32 v30, 16, v89
	v_and_b32_e32 v31, 0xffff0000, v89
	v_pk_mul_f32 v[20:21], v[20:21], s[0:1] op_sel_hi:[1,0]
	v_pk_fma_f32 v[26:27], v[26:27], v[28:29], v[30:31]
	v_cvt_f32_ubyte1_e32 v29, v83
	v_cvt_f32_ubyte0_e32 v28, v83
	v_lshlrev_b32_e32 v30, 16, v90
	v_and_b32_e32 v31, 0xffff0000, v90
	v_pk_mul_f32 v[22:23], v[22:23], s[0:1] op_sel_hi:[1,0]
	v_pk_fma_f32 v[28:29], v[20:21], v[28:29], v[30:31]
	v_cvt_f32_ubyte3_e32 v21, v83
	v_cvt_f32_ubyte2_e32 v20, v83
	v_lshlrev_b32_e32 v30, 16, v91
	v_and_b32_e32 v31, 0xffff0000, v91
	v_pk_fma_f32 v[30:31], v[22:23], v[20:21], v[30:31]
	v_cvt_pk_bf16_f32 v20, v24, v25
	v_cvt_pk_bf16_f32 v21, v26, v27
	v_cvt_pk_bf16_f32 v22, v28, v29
	v_cvt_pk_bf16_f32 v23, v30, v31
	global_store_dwordx4 v[32:33], v[20:23], off offset:256
	v_pk_mul_f32 v[16:17], v[16:17], s[0:1] op_sel_hi:[1,0]
	v_pk_mul_f32 v[18:19], v[18:19], s[0:1] op_sel_hi:[1,0]
	s_waitcnt vmcnt(6)
	v_cvt_f32_ubyte1_e32 v21, v68
	v_cvt_f32_ubyte0_e32 v20, v68
	v_lshlrev_b32_e32 v22, 16, v76
	v_and_b32_e32 v23, 0xffff0000, v76
	v_pk_fma_f32 v[16:17], v[16:17], v[20:21], v[22:23]
	v_cvt_f32_ubyte3_e32 v21, v68
	v_cvt_f32_ubyte2_e32 v20, v68
	v_lshlrev_b32_e32 v22, 16, v77
	v_and_b32_e32 v23, 0xffff0000, v77
	v_pk_mul_f32 v[12:13], v[12:13], s[0:1] op_sel_hi:[1,0]
	v_pk_fma_f32 v[18:19], v[18:19], v[20:21], v[22:23]
	v_cvt_f32_ubyte1_e32 v21, v69
	v_cvt_f32_ubyte0_e32 v20, v69
	v_lshlrev_b32_e32 v22, 16, v78
	v_and_b32_e32 v23, 0xffff0000, v78
	v_pk_mul_f32 v[14:15], v[14:15], s[0:1] op_sel_hi:[1,0]
	v_pk_fma_f32 v[20:21], v[12:13], v[20:21], v[22:23]
	v_cvt_f32_ubyte3_e32 v13, v69
	v_cvt_f32_ubyte2_e32 v12, v69
	v_lshlrev_b32_e32 v22, 16, v79
	v_and_b32_e32 v23, 0xffff0000, v79
	v_pk_fma_f32 v[22:23], v[14:15], v[12:13], v[22:23]
	v_cvt_pk_bf16_f32 v12, v16, v17
	v_mad_i64_i32 v[16:17], s[4:5], v114, s81, v[60:61]
	v_cvt_pk_bf16_f32 v13, v18, v19
	v_cvt_pk_bf16_f32 v14, v20, v21
	v_cvt_pk_bf16_f32 v15, v22, v23
	v_lshl_add_u64 v[16:17], v[16:17], 0, v[126:127]
	global_store_dwordx4 v[16:17], v[12:15], off
	v_pk_mul_f32 v[8:9], v[8:9], s[0:1] op_sel_hi:[1,0]
	v_pk_mul_f32 v[10:11], v[10:11], s[0:1] op_sel_hi:[1,0]
	v_cvt_f32_ubyte1_e32 v13, v70
	v_cvt_f32_ubyte0_e32 v12, v70
	v_lshlrev_b32_e32 v14, 16, v72
	v_and_b32_e32 v15, 0xffff0000, v72
	v_pk_fma_f32 v[8:9], v[8:9], v[12:13], v[14:15]
	v_cvt_f32_ubyte3_e32 v13, v70
	v_cvt_f32_ubyte2_e32 v12, v70
	v_lshlrev_b32_e32 v14, 16, v73
	v_and_b32_e32 v15, 0xffff0000, v73
	v_pk_mul_f32 v[4:5], v[4:5], s[0:1] op_sel_hi:[1,0]
	v_pk_fma_f32 v[10:11], v[10:11], v[12:13], v[14:15]
	v_cvt_f32_ubyte1_e32 v13, v71
	v_cvt_f32_ubyte0_e32 v12, v71
	v_lshlrev_b32_e32 v14, 16, v74
	v_and_b32_e32 v15, 0xffff0000, v74
	v_pk_mul_f32 v[6:7], v[6:7], s[0:1] op_sel_hi:[1,0]
	v_pk_fma_f32 v[12:13], v[4:5], v[12:13], v[14:15]
	v_cvt_f32_ubyte3_e32 v5, v71
	v_cvt_f32_ubyte2_e32 v4, v71
	v_lshlrev_b32_e32 v14, 16, v75
	v_and_b32_e32 v15, 0xffff0000, v75
	v_pk_fma_f32 v[14:15], v[6:7], v[4:5], v[14:15]
	v_cvt_pk_bf16_f32 v4, v8, v9
	v_cvt_pk_bf16_f32 v5, v10, v11
	v_cvt_pk_bf16_f32 v6, v12, v13
	v_cvt_pk_bf16_f32 v7, v14, v15
	global_store_dwordx4 v[16:17], v[4:7], off offset:256
	s_and_b64 vcc, exec, s[6:7]
	s_mov_b64 s[4:5], -1
	s_cbranch_vccnz .LBB0_582
	s_andn2_b64 vcc, exec, s[10:11]
	s_cbranch_vccnz .LBB0_581
	s_mov_b32 s98, 1
	s_branch .LBB0_581

;     __device__ bool next(int i, Unit& u) const { const int rounds = nwg / G; if (i >= rounds) return false; return StaticOrder::next(rounds - 1 - i, u); }
;     __device__ bool next(int i, Unit& u) const { const int rounds = nwg / G; if (i >= 2 * rounds) return false; const bool ok = StaticOrder::next(i >= rounds ? i - rounds : i, u); u.z = (i >= rounds) ? 1 : 0; return ok; }
; template <class Epi, class Sched, bool ALIGN_EPI = false, bool SP2 = false>
; __device__ __forceinline__ void gemm_phase(PG8_LAS unsigned char* lds, const Gemm g, const Sched& S, const Epi& E) {
;     ...
;         const bool has_next = S.next(ui + 1, nxt);
;         const char* nA = has_next ? (const char*)S.opA(g, nxt) + (size_t)nxt.pm * tstepA : cA; const char* nB = has_next ? (const char*)S.opB(g, nxt) + (size_t)nxt.pn * tstepB : cB;
.LBB0_699:
	s_ashr_i32 s19, s18, 31
	s_lshl_b64 s[4:5], s[18:19], 20
	v_readlane_b32 s22, v254, 33
	v_readlane_b32 s23, v254, 34
	s_add_u32 s22, s22, s4
	s_addc_u32 s23, s23, s5
	s_cmp_eq_u32 s98, 1
	s_cbranch_scc0 .Llr_out
	s_barrier
	s_mov_b32 s98, 0
.Llr_out:
	s_add_i32 s33, 0, 0x10000
	s_add_i32 s41, 0, 0x14000
	v_add_u32_e32 v116, s33, v176
	v_add_u32_e32 v117, s41, v176
	ds_read_b128 v[4:7], v116
	ds_read_b128 v[8:11], v116 offset:1024
	ds_read_b128 v[12:15], v116 offset:2048
	ds_read_b128 v[16:19], v116 offset:3072
	ds_read_b128 v[20:23], v117
	ds_read_b128 v[24:27], v117 offset:1024
	ds_read_b128 v[28:31], v117 offset:2048
	ds_read_b128 v[32:35], v117 offset:3072
	s_and_b64 s[4:5], s[10:11], exec
	s_cselect_b32 s3, s23, s25
	s_cselect_b32 s4, s22, s24
	v_lshl_add_u64 v[208:209], s[26:27], 0, v[162:163]
	s_mov_b64 s[10:11], 0x84080
	s_add_i32 s5, s29, 0xc000
	v_lshl_add_u64 v[68:69], v[208:209], 0, s[10:11]
	s_mov_b32 m0, s5
	s_mov_b64 s[10:11], 0xc6080
	s_add_i32 s19, s29, 0xe000
	ds_read_b128 v[36:39], v178
	ds_read_b128 v[40:43], v178 offset:1024
	ds_read_b128 v[44:47], v178 offset:2048
	ds_read_b128 v[48:51], v178 offset:3072
	ds_read_b128 v[52:55], v178 offset:4096
	ds_read_b128 v[56:59], v178 offset:5120
	ds_read_b128 v[60:63], v178 offset:6144
	ds_read_b128 v[64:67], v178 offset:7168
	global_load_lds_dwordx4 v[68:69], off
	v_lshl_add_u64 v[68:69], v[208:209], 0, s[10:11]
	s_mov_b32 m0, s19
	s_nop 0
	global_load_lds_dwordx4 v[68:69], off
	s_waitcnt vmcnt(16)
	s_waitcnt lgkmcnt(0)
	s_barrier
	s_setprio 1
	s_waitcnt lgkmcnt(0)
	v_mfma_f32_16x16x32_bf16 v[92:95], v[4:7], v[60:63], 0
	v_mfma_f32_16x16x32_bf16 v[68:71], v[4:7], v[36:39], 0
	v_mfma_f32_16x16x32_bf16 v[72:75], v[12:15], v[36:39], 0
	v_mfma_f32_16x16x32_bf16 v[76:79], v[4:7], v[44:47], 0
	v_mfma_f32_16x16x32_bf16 v[80:83], v[12:15], v[44:47], 0
	v_mfma_f32_16x16x32_bf16 v[84:87], v[4:7], v[52:55], 0
	v_mfma_f32_16x16x32_bf16 v[88:91], v[12:15], v[52:55], 0
	v_mfma_f32_16x16x32_bf16 v[100:103], v[8:11], v[64:67], v[92:95]
	v_mfma_f32_16x16x32_bf16 v[92:95], v[12:15], v[60:63], 0
	v_mfma_f32_16x16x32_bf16 v[68:71], v[8:11], v[40:43], v[68:71]
	v_mfma_f32_16x16x32_bf16 v[72:75], v[16:19], v[40:43], v[72:75]
	v_mfma_f32_16x16x32_bf16 v[76:79], v[8:11], v[48:51], v[76:79]
	v_mfma_f32_16x16x32_bf16 v[80:83], v[16:19], v[48:51], v[80:83]
	v_mfma_f32_16x16x32_bf16 v[84:87], v[8:11], v[56:59], v[84:87]
	v_mfma_f32_16x16x32_bf16 v[88:91], v[16:19], v[56:59], v[88:91]
	v_mfma_f32_16x16x32_bf16 v[104:107], v[16:19], v[64:67], v[92:95]
	s_setprio 0
	s_setprio 1
	v_mfma_f32_16x16x32_bf16 v[92:95], v[20:23], v[36:39], 0
	v_mfma_f32_16x16x32_bf16 v[36:39], v[28:31], v[36:39], 0
	v_mfma_f32_16x16x32_bf16 v[120:123], v[24:27], v[40:43], v[92:95]
	v_mfma_f32_16x16x32_bf16 v[36:39], v[32:35], v[40:43], v[36:39]
	v_mfma_f32_16x16x32_bf16 v[40:43], v[20:23], v[44:47], 0
	v_mfma_f32_16x16x32_bf16 v[44:47], v[28:31], v[44:47], 0
	v_mfma_f32_16x16x32_bf16 v[40:43], v[24:27], v[48:51], v[40:43]
	v_mfma_f32_16x16x32_bf16 v[44:47], v[32:35], v[48:51], v[44:47]
	v_mfma_f32_16x16x32_bf16 v[48:51], v[20:23], v[52:55], 0
	v_mfma_f32_16x16x32_bf16 v[52:55], v[28:31], v[52:55], 0
	v_mfma_f32_16x16x32_bf16 v[48:51], v[24:27], v[56:59], v[48:51]
	v_mfma_f32_16x16x32_bf16 v[52:55], v[32:35], v[56:59], v[52:55]
	v_mfma_f32_16x16x32_bf16 v[56:59], v[20:23], v[60:63], 0
	v_mfma_f32_16x16x32_bf16 v[60:63], v[28:31], v[60:63], 0
	v_mfma_f32_16x16x32_bf16 v[56:59], v[24:27], v[64:67], v[56:59]
	v_mfma_f32_16x16x32_bf16 v[60:63], v[32:35], v[64:67], v[60:63]
	s_setprio 0
	s_barrier
	v_lshl_add_u64 v[250:251], s[24:25], 0, v[160:161]
	s_mov_b64 s[10:11], 0x100
	s_add_i32 s33, s33, s28
	v_lshl_add_u64 v[118:119], v[250:251], 0, s[10:11]
	s_mov_b32 m0, s33
	s_mov_b64 s[42:43], 0x40100
	s_add_i32 s40, s33, 0x2000
	ds_read_b128 v[64:67], v178 offset:16384
	ds_read_b128 v[92:95], v178 offset:17408
	ds_read_b128 v[96:99], v178 offset:18432
	ds_read_b128 v[108:111], v178 offset:19456
	ds_read_b128 v[112:115], v178 offset:20480
	ds_read_b128 v[124:127], v178 offset:21504
	ds_read_b128 v[128:131], v178 offset:22528
	ds_read_b128 v[132:135], v178 offset:23552
	global_load_lds_dwordx4 v[118:119], off
	v_lshl_add_u64 v[118:119], v[250:251], 0, s[42:43]
	s_mov_b32 m0, s40
	s_mov_b64 s[42:43], 0x80100
	s_add_i32 s41, s41, s28
	global_load_lds_dwordx4 v[118:119], off
	v_lshl_add_u64 v[118:119], v[250:251], 0, s[42:43]
	s_mov_b32 m0, s41
	s_mov_b64 s[42:43], 0xc0100
	global_load_lds_dwordx4 v[118:119], off
	v_lshl_add_u64 v[118:119], v[250:251], 0, s[42:43]
	s_add_i32 s42, s41, 0x2000
	s_mov_b32 m0, s42
	s_nop 0
	global_load_lds_dwordx4 v[118:119], off
	v_lshl_add_u64 v[118:119], v[208:209], 0, s[10:11]
	s_mov_b32 m0, s29
	s_mov_b64 s[10:11], 0x42100
	global_load_lds_dwordx4 v[118:119], off
	v_lshl_add_u64 v[118:119], v[208:209], 0, s[10:11]
	s_mov_b32 m0, s30
	s_nop 0
	global_load_lds_dwordx4 v[118:119], off
	s_waitcnt vmcnt(16)
	s_waitcnt lgkmcnt(0)
	s_barrier
	s_setprio 1
	s_waitcnt lgkmcnt(0)
	v_mfma_f32_16x16x32_bf16 v[136:139], v[4:7], v[64:67], 0
	v_mfma_f32_16x16x32_bf16 v[144:147], v[8:11], v[92:95], v[136:139]
	v_mfma_f32_16x16x32_bf16 v[136:139], v[12:15], v[64:67], 0
	v_mfma_f32_16x16x32_bf16 v[148:151], v[16:19], v[92:95], v[136:139]
	v_mfma_f32_16x16x32_bf16 v[136:139], v[4:7], v[96:99], 0
	v_mfma_f32_16x16x32_bf16 v[152:155], v[8:11], v[108:111], v[136:139]
	v_mfma_f32_16x16x32_bf16 v[136:139], v[12:15], v[96:99], 0
	v_mfma_f32_16x16x32_bf16 v[156:159], v[16:19], v[108:111], v[136:139]
	v_mfma_f32_16x16x32_bf16 v[136:139], v[4:7], v[112:115], 0
	v_mfma_f32_16x16x32_bf16 v[4:7], v[4:7], v[128:131], 0
	v_mfma_f32_16x16x32_bf16 v[166:169], v[8:11], v[124:127], v[136:139]
	v_mfma_f32_16x16x32_bf16 v[4:7], v[8:11], v[132:135], v[4:7]
	v_mfma_f32_16x16x32_bf16 v[8:11], v[12:15], v[128:131], 0
	v_mfma_f32_16x16x32_bf16 v[136:139], v[12:15], v[112:115], 0
	v_mfma_f32_16x16x32_bf16 v[8:11], v[16:19], v[132:135], v[8:11]
	v_mfma_f32_16x16x32_bf16 v[170:173], v[16:19], v[124:127], v[136:139]
	s_setprio 0
	s_setprio 1
	v_mfma_f32_16x16x32_bf16 v[12:15], v[20:23], v[64:67], 0
	v_mfma_f32_16x16x32_bf16 v[180:183], v[24:27], v[92:95], v[12:15]
	v_mfma_f32_16x16x32_bf16 v[12:15], v[28:31], v[64:67], 0
	v_mfma_f32_16x16x32_bf16 v[184:187], v[32:35], v[92:95], v[12:15]
	v_mfma_f32_16x16x32_bf16 v[12:15], v[20:23], v[96:99], 0
	v_mfma_f32_16x16x32_bf16 v[188:191], v[24:27], v[108:111], v[12:15]
	v_mfma_f32_16x16x32_bf16 v[12:15], v[28:31], v[96:99], 0
	v_mfma_f32_16x16x32_bf16 v[192:195], v[32:35], v[108:111], v[12:15]
	v_mfma_f32_16x16x32_bf16 v[12:15], v[20:23], v[112:115], 0
	v_mfma_f32_16x16x32_bf16 v[196:199], v[24:27], v[124:127], v[12:15]
	v_mfma_f32_16x16x32_bf16 v[12:15], v[28:31], v[112:115], 0
	v_mfma_f32_16x16x32_bf16 v[200:203], v[32:35], v[124:127], v[12:15]
	v_mfma_f32_16x16x32_bf16 v[12:15], v[20:23], v[128:131], 0
	v_mfma_f32_16x16x32_bf16 v[204:207], v[24:27], v[132:135], v[12:15]
	v_mfma_f32_16x16x32_bf16 v[12:15], v[28:31], v[128:131], 0
	v_mfma_f32_16x16x32_bf16 v[132:135], v[32:35], v[132:135], v[12:15]
	s_setprio 0
	s_barrier
	s_add_i32 s43, 0, 0x18000
	s_add_i32 s45, 0, 0x1c000
	v_add_u32_e32 v118, s43, v176
	v_add_u32_e32 v119, s45, v176
	s_nop 0
	ds_read_b128 v[12:15], v118
	ds_read_b128 v[16:19], v118 offset:1024
	ds_read_b128 v[20:23], v118 offset:2048
	ds_read_b128 v[24:27], v118 offset:3072
	ds_read_b128 v[214:217], v119
	ds_read_b128 v[218:221], v119 offset:1024
	ds_read_b128 v[222:225], v119 offset:2048
	ds_read_b128 v[226:229], v119 offset:3072
	s_mov_b64 s[10:11], 0x84100
	s_mov_b32 m0, s31
	v_lshl_add_u64 v[92:93], v[208:209], 0, s[10:11]
	s_mov_b64 s[10:11], 0xc6100
	ds_read_b128 v[28:31], v178 offset:32768
	ds_read_b128 v[32:35], v178 offset:33792
	ds_read_b128 v[64:67], v178 offset:34816
	ds_read_b128 v[230:233], v178 offset:35840
	ds_read_b128 v[234:237], v178 offset:36864
	ds_read_b128 v[238:241], v178 offset:37888
	ds_read_b128 v[242:245], v178 offset:38912
	ds_read_b128 v[246:249], v178 offset:39936
	global_load_lds_dwordx4 v[92:93], off
	v_lshl_add_u64 v[92:93], v[208:209], 0, s[10:11]
	s_mov_b32 m0, s34
	s_nop 0
	global_load_lds_dwordx4 v[92:93], off
	s_waitcnt vmcnt(8)
	s_waitcnt lgkmcnt(0)
	s_barrier
	s_setprio 1
	s_waitcnt lgkmcnt(0)
	v_mfma_f32_16x16x32_bf16 v[68:71], v[12:15], v[28:31], v[68:71]
	v_mfma_f32_16x16x32_bf16 v[140:143], v[16:19], v[32:35], v[68:71]
	v_mfma_f32_16x16x32_bf16 v[68:71], v[20:23], v[28:31], v[72:75]
	v_mfma_f32_16x16x32_bf16 v[136:139], v[24:27], v[32:35], v[68:71]
	v_mfma_f32_16x16x32_bf16 v[68:71], v[12:15], v[64:67], v[76:79]
	v_mfma_f32_16x16x32_bf16 v[112:115], v[16:19], v[230:233], v[68:71]
	v_mfma_f32_16x16x32_bf16 v[68:71], v[20:23], v[64:67], v[80:83]
	v_mfma_f32_16x16x32_bf16 v[108:111], v[24:27], v[230:233], v[68:71]
	v_mfma_f32_16x16x32_bf16 v[68:71], v[12:15], v[234:237], v[84:87]
	v_mfma_f32_16x16x32_bf16 v[96:99], v[16:19], v[238:241], v[68:71]
	v_mfma_f32_16x16x32_bf16 v[68:71], v[20:23], v[234:237], v[88:91]
	v_mfma_f32_16x16x32_bf16 v[92:95], v[24:27], v[238:241], v[68:71]
	v_mfma_f32_16x16x32_bf16 v[68:71], v[12:15], v[242:245], v[100:103]
	v_mfma_f32_16x16x32_bf16 v[80:83], v[16:19], v[246:249], v[68:71]
	v_mfma_f32_16x16x32_bf16 v[68:71], v[20:23], v[242:245], v[104:107]
	v_mfma_f32_16x16x32_bf16 v[76:79], v[24:27], v[246:249], v[68:71]
	s_setprio 0
	s_setprio 1
	v_mfma_f32_16x16x32_bf16 v[68:71], v[214:217], v[28:31], v[120:123]
	v_mfma_f32_16x16x32_bf16 v[28:31], v[222:225], v[28:31], v[36:39]
	v_mfma_f32_16x16x32_bf16 v[124:127], v[226:229], v[32:35], v[28:31]
	v_mfma_f32_16x16x32_bf16 v[28:31], v[214:217], v[64:67], v[40:43]
	v_mfma_f32_16x16x32_bf16 v[104:107], v[218:221], v[230:233], v[28:31]
	v_mfma_f32_16x16x32_bf16 v[28:31], v[222:225], v[64:67], v[44:47]
	v_mfma_f32_16x16x32_bf16 v[100:103], v[226:229], v[230:233], v[28:31]
	v_mfma_f32_16x16x32_bf16 v[28:31], v[214:217], v[234:237], v[48:51]
	v_mfma_f32_16x16x32_bf16 v[88:91], v[218:221], v[238:241], v[28:31]
	v_mfma_f32_16x16x32_bf16 v[28:31], v[222:225], v[234:237], v[52:55]
	v_mfma_f32_16x16x32_bf16 v[84:87], v[226:229], v[238:241], v[28:31]
	v_mfma_f32_16x16x32_bf16 v[28:31], v[214:217], v[242:245], v[56:59]
	v_mfma_f32_16x16x32_bf16 v[72:75], v[218:221], v[246:249], v[28:31]
	v_mfma_f32_16x16x32_bf16 v[28:31], v[222:225], v[242:245], v[60:63]
	v_mfma_f32_16x16x32_bf16 v[128:131], v[218:221], v[32:35], v[68:71]
	v_mfma_f32_16x16x32_bf16 v[68:71], v[226:229], v[246:249], v[28:31]
	s_setprio 0
	s_barrier
; #define PG8_MMA(ai, bj, At, Bt) do { __builtin_amdgcn_s_setprio(1); _Pragma("unroll") for (int m = 0; m < 4; ++m) _Pragma("unroll") for (int n = 0; n < 2; ++n) _Pragma("unroll") for (int k = 0; k < 2; ++k) \
;         acc[ai][bj][m][n] = __builtin_amdgcn_mfma_f32_16x16x32_bf16(Bt[n][k], At[m][k], acc[ai][bj][m][n], 0, 0, 0); __builtin_amdgcn_s_setprio(0); } while (0)
; #define PG8_WAIT_V(n) asm volatile("s_waitcnt vmcnt(" #n ")" ::: "memory")
; #define PG8_TRIP_HEAD(T) const int t = (T); const bool last = (t == nt - 2); \
;             const char* a1 = cA + (size_t)(t + 1) * kstep; \
;             const char* a2 = last ? nA : cA + (size_t)(t + 2) * kstep; const char* b2 = last ? nB : cB + (size_t)(t + 2) * kstep; \
;             const char* a3 = a2 + kstep; const char* b3 = b2 + kstep; \
;             if (last && has_next) S.a_ready(nxt);
; template <class Epi, class Sched, bool ALIGN_EPI = false, bool SP2 = false>
; __device__ __forceinline__ void gemm_phase(PG8_LAS unsigned char* lds, const Gemm g, const Sched& S, const Epi& E) {
;     ...
;         if constexpr (SP2) {
;             { PG8_TRIP_HEAD(0) PG8_TRIP_SP2(asm volatile("s_waitcnt vmcnt(%0)" :: "n"(8 + Epi::NST) : "memory"), PG8_MMAZ) }
;             for (int tt = 2; tt < nt; tt += 2) { PG8_TRIP_HEAD(tt) PG8_TRIP_SP2(PG8_WAIT_V(8), PG8_MMA) }
	s_mov_b64 s[10:11], 0x180
	s_add_i32 s43, s43, s28
	s_nop 1
	v_lshl_add_u64 v[28:29], v[250:251], 0, s[10:11]
	s_mov_b32 m0, s43
	s_mov_b64 s[46:47], 0x40180
	s_add_i32 s44, s43, 0x2000
	ds_read_b128 v[36:39], v178 offset:49152
	ds_read_b128 v[40:43], v178 offset:50176
	ds_read_b128 v[120:123], v178 offset:51200
	ds_read_b128 v[230:233], v178 offset:52224
	ds_read_b128 v[234:237], v178 offset:53248
	ds_read_b128 v[238:241], v178 offset:54272
	ds_read_b128 v[242:245], v178 offset:55296
	ds_read_b128 v[246:249], v178 offset:56320
	global_load_lds_dwordx4 v[28:29], off
	v_lshl_add_u64 v[28:29], v[250:251], 0, s[46:47]
	s_mov_b32 m0, s44
	s_mov_b64 s[46:47], 0x80180
	s_add_i32 s45, s45, s28
	global_load_lds_dwordx4 v[28:29], off
	v_lshl_add_u64 v[28:29], v[250:251], 0, s[46:47]
	s_mov_b32 m0, s45
	s_mov_b64 s[46:47], 0xc0180
	global_load_lds_dwordx4 v[28:29], off
	v_lshl_add_u64 v[28:29], v[250:251], 0, s[46:47]
	s_add_i32 s46, s45, 0x2000
	s_mov_b32 m0, s46
	s_nop 0
	global_load_lds_dwordx4 v[28:29], off
	v_lshl_add_u64 v[28:29], v[208:209], 0, s[10:11]
	s_mov_b32 m0, s36
	s_mov_b64 s[10:11], 0x42180
	global_load_lds_dwordx4 v[28:29], off
	v_lshl_add_u64 v[28:29], v[208:209], 0, s[10:11]
	s_mov_b32 m0, s37
	s_nop 0
	global_load_lds_dwordx4 v[28:29], off
	s_waitcnt vmcnt(8)
	s_waitcnt lgkmcnt(0)
	s_barrier
	s_setprio 1
	s_waitcnt lgkmcnt(0)
	v_mfma_f32_16x16x32_bf16 v[28:31], v[12:15], v[36:39], v[144:147]
	v_mfma_f32_16x16x32_bf16 v[56:59], v[16:19], v[40:43], v[28:31]
	v_mfma_f32_16x16x32_bf16 v[28:31], v[20:23], v[36:39], v[148:151]
	v_mfma_f32_16x16x32_bf16 v[52:55], v[24:27], v[40:43], v[28:31]
	v_mfma_f32_16x16x32_bf16 v[28:31], v[12:15], v[120:123], v[152:155]
	v_mfma_f32_16x16x32_bf16 v[48:51], v[16:19], v[230:233], v[28:31]
	v_mfma_f32_16x16x32_bf16 v[28:31], v[20:23], v[120:123], v[156:159]
	v_mfma_f32_16x16x32_bf16 v[44:47], v[24:27], v[230:233], v[28:31]
	v_mfma_f32_16x16x32_bf16 v[28:31], v[12:15], v[234:237], v[166:169]
	v_mfma_f32_16x16x32_bf16 v[4:7], v[12:15], v[242:245], v[4:7]
	v_mfma_f32_16x16x32_bf16 v[32:35], v[16:19], v[238:241], v[28:31]
	v_mfma_f32_16x16x32_bf16 v[28:31], v[20:23], v[234:237], v[170:173]
	v_mfma_f32_16x16x32_bf16 v[16:19], v[16:19], v[246:249], v[4:7]
	v_mfma_f32_16x16x32_bf16 v[4:7], v[20:23], v[242:245], v[8:11]
	v_mfma_f32_16x16x32_bf16 v[28:31], v[24:27], v[238:241], v[28:31]
	v_mfma_f32_16x16x32_bf16 v[12:15], v[24:27], v[246:249], v[4:7]
	s_setprio 0
	s_setprio 1
	v_mfma_f32_16x16x32_bf16 v[4:7], v[214:217], v[36:39], v[180:183]
	v_mfma_f32_16x16x32_bf16 v[64:67], v[218:221], v[40:43], v[4:7]
	v_mfma_f32_16x16x32_bf16 v[4:7], v[222:225], v[36:39], v[184:187]
	v_mfma_f32_16x16x32_bf16 v[60:63], v[226:229], v[40:43], v[4:7]
	v_mfma_f32_16x16x32_bf16 v[4:7], v[214:217], v[120:123], v[188:191]
	v_mfma_f32_16x16x32_bf16 v[40:43], v[218:221], v[230:233], v[4:7]
	v_mfma_f32_16x16x32_bf16 v[4:7], v[222:225], v[120:123], v[192:195]
	v_mfma_f32_16x16x32_bf16 v[36:39], v[226:229], v[230:233], v[4:7]
	v_mfma_f32_16x16x32_bf16 v[4:7], v[214:217], v[234:237], v[196:199]
	v_mfma_f32_16x16x32_bf16 v[24:27], v[218:221], v[238:241], v[4:7]
	v_mfma_f32_16x16x32_bf16 v[4:7], v[222:225], v[234:237], v[200:203]
	v_mfma_f32_16x16x32_bf16 v[20:23], v[226:229], v[238:241], v[4:7]
	v_mfma_f32_16x16x32_bf16 v[4:7], v[214:217], v[242:245], v[204:207]
	v_mfma_f32_16x16x32_bf16 v[8:11], v[218:221], v[246:249], v[4:7]
	v_mfma_f32_16x16x32_bf16 v[4:7], v[222:225], v[242:245], v[132:135]
	v_mfma_f32_16x16x32_bf16 v[4:7], v[226:229], v[246:249], v[4:7]
	s_setprio 0
	s_barrier
	s_add_u32 s10, s26, 0x84180
	s_addc_u32 s11, s27, 0
	s_add_u32 s24, s24, 0x200
	s_addc_u32 s25, s25, 0
	s_mov_b32 s26, 0
	s_mov_b64 s[52:53], 0x80000
	s_mov_b64 s[54:55], 0x80080
	s_mov_b64 s[56:57], 0xc0000
	s_mov_b64 s[60:61], 0xc0080
	s_mov_b64 s[62:63], 0xc6000

; #define PG8_BAR __builtin_amdgcn_s_barrier()
;     __device__ __forceinline__ void operator()(const f32x4 (&acc)[2][2][4][2], const Unit& u, int wr, int wc, int fr, int fq) const {
;     ...
;             { const float sv = (fq == 0) ? ssm[0] : (fq == 1) ? ssm[1] : (fq == 2) ? ssm[2] : ssm[3];
;               ssq[(size_t)(row0 + ai * HALF + fq * 16) * 32 + u.pn * 4 + wc] = sv; }
; template <class Epi, class Sched, bool ALIGN_EPI = false, bool SP2 = false>
; __device__ __forceinline__ void gemm_phase(PG8_LAS unsigned char* lds, const Gemm g, const Sched& S, const Epi& E) {
;     ...
;         if (!has_next) break;
;         if constexpr (!SP2) {
; #pragma unroll
;         for (int a = 0; a < 2; ++a)
; #pragma unroll
;             for (int b = 0; b < 2; ++b)
; #pragma unroll
;                 for (int m = 0; m < 4; ++m)
; #pragma unroll
;                     for (int n = 0; n < 2; ++n) acc[a][b][m][n] = (f32x4){0.f, 0.f, 0.f, 0.f};
;         }
;         cur = nxt; cA = nA; cB = nB; ++ui;
;         if constexpr (ALIGN_EPI) { if (wr == 1) PG8_BAR; }
.LBB0_719:
	s_or_b64 exec, exec, s[4:5]
	s_waitcnt lgkmcnt(0)
	v_add_u32_e32 v6, 0x80, v92
	v_ashrrev_i32_e32 v7, 31, v6
	v_lshlrev_b64 v[6:7], 7, v[6:7]
	v_lshl_add_u64 v[6:7], s[14:15], 0, v[6:7]
	v_lshl_add_u64 v[6:7], s[10:11], 2, v[6:7]
	v_lshl_add_u64 v[6:7], v[6:7], 0, s[0:1]
	global_store_dword v[6:7], v4, off
	s_and_b64 vcc, exec, s[8:9]
	s_mov_b64 s[4:5], -1
	s_cbranch_vccnz .LBB0_690
	s_andn2_b64 vcc, exec, s[12:13]
	s_cbranch_vccnz .LBB0_689
	s_mov_b32 s98, 1
	s_branch .LBB0_689
